# v64 + cache policy: thin passes load y/h with nt and store the residual (and the final f32 out) with sc1 nt; u stores unchanged
# baseline (speedup 1.0000x reference)
; __device__ __forceinline__ void thin_pass(const Ctx& C, const bf16* hin, bf16* hout, bf16* u, float* out, const bf16* y, const float* gpost, float cmul, const float* gpre, bool last) {
;     ...
;     for (int m0 = mstart; m0 < mend; m0 += mstep) {
;         v4u yr[RB][2], hr[RB][2];
; #pragma unroll
;         for (int b = 0; b < RB; ++b) { const v4u* yp = (const v4u*)(y + (size_t)(m0 + b) * D); const v4u* hp = (const v4u*)(hin + (size_t)(m0 + b) * D);
;             yr[b][0] = yp[lane]; yr[b][1] = yp[64 + lane]; hr[b][0] = hp[lane]; hr[b][1] = hp[64 + lane]; }
; #pragma unroll
;         for (int b = 0; b < RB; ++b) {
;             const int m = m0 + b; const v4u y0 = yr[b][0], y1 = yr[b][1], h0 = hr[b][0], h1 = hr[b][1];
;             f32x4 yv[4], h[4];
;             yv[0] = (f32x4){bf_lo(y0.x), bf_hi(y0.x), bf_lo(y0.y), bf_hi(y0.y)}; yv[1] = (f32x4){bf_lo(y0.z), bf_hi(y0.z), bf_lo(y0.w), bf_hi(y0.w)};
;             yv[2] = (f32x4){bf_lo(y1.x), bf_hi(y1.x), bf_lo(y1.y), bf_hi(y1.y)}; yv[3] = (f32x4){bf_lo(y1.z), bf_hi(y1.z), bf_lo(y1.w), bf_hi(y1.w)};
;             h[0] = (f32x4){bf_lo(h0.x), bf_hi(h0.x), bf_lo(h0.y), bf_hi(h0.y)}; h[1] = (f32x4){bf_lo(h0.z), bf_hi(h0.z), bf_lo(h0.w), bf_hi(h0.w)};
;             h[2] = (f32x4){bf_lo(h1.x), bf_hi(h1.x), bf_lo(h1.y), bf_hi(h1.y)}; h[3] = (f32x4){bf_lo(h1.z), bf_hi(h1.z), bf_lo(h1.w), bf_hi(h1.w)};
;             float ss = 0.f;
; #pragma unroll
;             for (int i = 0; i < 4; ++i) ss += (yv[i][0] * yv[i][0] + yv[i][1] * yv[i][1]) + (yv[i][2] * yv[i][2] + yv[i][3] * yv[i][3]);
;             const float ry = cmul / sqrtf(wave_sum(ss) * (1.0f / D) + RMS_EPS);
; #pragma unroll
;             for (int i = 0; i < 4; ++i) h[i] = h[i] + yv[i] * ry * g4[i];
.LBB0_734:
	v_lshl_add_u64 v[114:115], s[14:15], 0, v[100:101]
	v_add_co_u32_e32 v38, vcc, 0xd000000, v114
	v_lshl_add_u64 v[36:37], s[20:21], 0, v[100:101]
	s_nop 0
	v_addc_co_u32_e32 v39, vcc, 0, v115, vcc
	flat_load_dwordx4 v[84:87], v[36:37] nt
	flat_load_dwordx4 v[88:91], v[36:37] offset:1024 nt
	flat_load_dwordx4 v[92:95], v[38:39] offset:1024 nt
	flat_load_dwordx4 v[96:99], v[38:39] nt
	s_add_i32 s22, s10, 3
	flat_load_dwordx4 v[80:83], v[36:37] offset:2048 nt
	flat_load_dwordx4 v[68:71], v[36:37] offset:3072 nt
	v_add_co_u32_e32 v36, vcc, s84, v36
	s_ashr_i32 s23, s22, 31
	s_nop 0
	v_addc_co_u32_e32 v37, vcc, 0, v37, vcc
	v_add_co_u32_e32 v56, vcc, s91, v114
	s_lshl_b64 s[2:3], s[22:23], 11
	flat_load_dwordx4 v[64:67], v[36:37] nt
	flat_load_dwordx4 v[52:55], v[36:37] offset:1024 nt
	v_lshl_add_u64 v[36:37], v[102:103], 0, s[2:3]
	v_lshl_add_u64 v[58:59], v[104:105], 0, s[2:3]
	v_addc_co_u32_e32 v57, vcc, 0, v115, vcc
	flat_load_dwordx4 v[76:79], v[38:39] offset:2048 nt
	flat_load_dwordx4 v[72:75], v[38:39] offset:3072 nt
	flat_load_dwordx4 v[44:47], v[36:37] nt
	flat_load_dwordx4 v[40:43], v[36:37] offset:1024 nt
	flat_load_dwordx4 v[48:51], v[58:59] nt
	s_nop 0
	flat_load_dwordx4 v[36:39], v[58:59] offset:1024 nt
	flat_load_dwordx4 v[60:63], v[56:57] nt
	s_nop 0
	flat_load_dwordx4 v[56:59], v[56:57] offset:1024 nt
	s_waitcnt vmcnt(0) lgkmcnt(0)
	v_lshlrev_b32_e32 v118, 16, v86
	v_and_b32_e32 v119, 0xffff0000, v86
	v_lshlrev_b32_e32 v124, 16, v94
	v_and_b32_e32 v142, 0xffff0000, v94
	v_lshlrev_b32_e32 v86, 16, v96
	v_lshlrev_b32_e32 v94, 16, v97
	v_lshlrev_b32_e32 v120, 16, v87
	v_and_b32_e32 v121, 0xffff0000, v87
	v_lshlrev_b32_e32 v122, 16, v88
	v_and_b32_e32 v123, 0xffff0000, v88
	v_lshlrev_b32_e32 v126, 16, v95
	v_and_b32_e32 v127, 0xffff0000, v95
	v_and_b32_e32 v87, 0xffff0000, v96
	v_and_b32_e32 v95, 0xffff0000, v97
	v_lshlrev_b32_e32 v97, 16, v99
	v_lshlrev_b32_e32 v96, 16, v98
	v_and_b32_e32 v99, 0xffff0000, v99
	v_and_b32_e32 v98, 0xffff0000, v98
	v_mul_f32_e32 v2, v86, v86
	v_mul_f32_e32 v88, v94, v94
	v_lshlrev_b32_e32 v128, 16, v92
	v_and_b32_e32 v129, 0xffff0000, v92
	v_lshlrev_b32_e32 v92, 16, v93
	v_pk_mul_f32 v[130:131], v[98:99], v[98:99]
	v_pk_fma_f32 v[138:139], v[86:87], v[86:87], v[2:3] op_sel_hi:[1,1,0]
	v_pk_fma_f32 v[140:141], v[94:95], v[94:95], v[88:89] op_sel_hi:[1,1,0]
	v_and_b32_e32 v93, 0xffff0000, v93
	v_mul_f32_e32 v132, v128, v128
	v_mul_f32_e32 v134, v92, v92
	v_mov_b32_e32 v136, v124
	v_pk_fma_f32 v[130:131], v[96:97], v[96:97], v[130:131]
	v_mov_b32_e32 v125, v139
	v_mov_b32_e32 v137, v141
	v_pk_fma_f32 v[132:133], v[128:129], v[128:129], v[132:133] op_sel_hi:[1,1,0]
	v_pk_fma_f32 v[134:135], v[92:93], v[92:93], v[134:135] op_sel_hi:[1,1,0]
	v_pk_add_f32 v[130:131], v[130:131], v[130:131] op_sel_hi:[0,1]
	v_pk_add_f32 v[138:139], v[138:139], v[140:141]
	v_pk_mul_f32 v[136:137], v[124:125], v[136:137]
	v_mul_f32_e32 v132, v126, v126
	v_mul_f32_e32 v134, v127, v127
	v_mul_f32_e32 v130, v142, v142
	v_mov_b32_e32 v137, v139
	v_pk_add_f32 v[132:133], v[132:133], v[134:135]
	v_pk_add_f32 v[130:131], v[136:137], v[130:131]
	v_lshlrev_b32_e32 v134, 16, v91
	v_pk_add_f32 v[130:131], v[130:131], v[132:133]
	v_lshlrev_b32_e32 v132, 16, v90
	v_add_f32_e32 v2, v130, v131
	v_and_b32_e32 v135, 0xffff0000, v91
	v_lshlrev_b32_e32 v116, 16, v84
	v_add_f32_dpp v2, v2, v2 quad_perm:[1,0,3,2] row_mask:0xf bank_mask:0xf bound_ctrl:1
	v_and_b32_e32 v117, 0xffff0000, v84
	v_lshlrev_b32_e32 v84, 16, v85
	v_add_f32_dpp v2, v2, v2 quad_perm:[2,3,0,1] row_mask:0xf bank_mask:0xf bound_ctrl:1
	v_and_b32_e32 v85, 0xffff0000, v85
	s_nop 0
	v_add_f32_dpp v2, v2, v2 row_half_mirror row_mask:0xf bank_mask:0xf bound_ctrl:1
	s_nop 1
	v_add_f32_dpp v2, v2, v2 row_mirror row_mask:0xf bank_mask:0xf bound_ctrl:1
	s_nop 0
	v_readlane_b32 s1, v2, 16
	v_readlane_b32 s4, v2, 48
	v_readlane_b32 s2, v2, 0
	v_readlane_b32 s3, v2, 32
	v_mov_b32_e32 v130, s1
	v_mov_b32_e32 v131, s4
	v_pk_add_f32 v[130:131], s[2:3], v[130:131]
	s_mov_b64 s[4:5], -1
	v_add_f32_e32 v2, v130, v131
	v_fmamk_f32 v2, v2, 0x3a800000, v214
	v_lshlrev_b32_e32 v130, 16, v89
	v_and_b32_e32 v131, 0xffff0000, v89
	v_and_b32_e32 v133, 0xffff0000, v90
	v_rsq_f32_e32 v2, v2
	s_nop 0
	v_mul_f32_e32 v2, 0.5, v2
	v_pk_mul_f32 v[88:89], v[2:3], v[86:87] op_sel_hi:[0,1]
	v_pk_mul_f32 v[86:87], v[2:3], v[94:95] op_sel_hi:[0,1]
	v_pk_fma_f32 v[86:87], v[10:11], v[86:87], v[84:85]
	v_pk_fma_f32 v[84:85], v[8:9], v[88:89], v[116:117]
	v_mov_b32_e32 v88, v96
	v_mov_b32_e32 v89, v98
	v_mov_b32_e32 v98, v97
	v_pk_mul_f32 v[96:97], v[2:3], v[128:129] op_sel_hi:[0,1]
	v_pk_mul_f32 v[92:93], v[2:3], v[92:93] op_sel_hi:[0,1]
	v_mov_b32_e32 v125, v142
	v_pk_mul_f32 v[88:89], v[2:3], v[88:89] op_sel_hi:[0,1]
	v_pk_mul_f32 v[90:91], v[2:3], v[98:99] op_sel_hi:[0,1]
	v_pk_fma_f32 v[94:95], v[18:19], v[92:93], v[130:131]
	v_pk_fma_f32 v[92:93], v[16:17], v[96:97], v[122:123]
	v_pk_mul_f32 v[96:97], v[124:125], v[2:3] op_sel_hi:[1,0]
	v_pk_mul_f32 v[98:99], v[126:127], v[2:3] op_sel_hi:[1,0]
	v_cndmask_b32_e64 v2, 0, 1, s[6:7]
	v_pk_fma_f32 v[90:91], v[6:7], v[90:91], v[120:121]
	v_pk_fma_f32 v[88:89], v[4:5], v[88:89], v[118:119]
	v_pk_fma_f32 v[98:99], v[14:15], v[98:99], v[134:135]
	v_pk_fma_f32 v[96:97], v[12:13], v[96:97], v[132:133]
	v_cmp_ne_u32_e64 s[2:3], 1, v2
	s_andn2_b64 vcc, exec, s[6:7]
	v_lshl_add_u64 v[116:117], s[18:19], 0, v[100:101]
	s_cbranch_vccnz .LBB0_736
; __device__ __forceinline__ unsigned pk2(float lo, float hi) { unsigned r; asm("v_cvt_pk_bf16_f32 %0, %1, %2" : "=v"(r) : "v"(lo), "v"(hi)); return r; }
; __device__ __forceinline__ void thin_pass(const Ctx& C, const bf16* hin, bf16* hout, bf16* u, float* out, const bf16* y, const float* gpost, float cmul, const float* gpre, bool last) {
;     ...
;             if (last) { f32x4* op = (f32x4*)(out + (size_t)m * D); op[2 * lane] = h[0]; op[2 * lane + 1] = h[1]; op[128 + 2 * lane] = h[2]; op[128 + 2 * lane + 1] = h[3]; }
;             else {
;                 float s2 = 0.f;
; #pragma unroll
;                 for (int i = 0; i < 4; ++i) s2 += (h[i][0] * h[i][0] + h[i][1] * h[i][1]) + (h[i][2] * h[i][2] + h[i][3] * h[i][3]);
;                 const float rh = 1.0f / sqrtf(wave_sum(s2) * (1.0f / D) + RMS_EPS);
;                 v4u o0, o1; o0.x = pk2(h[0][0], h[0][1]); o0.y = pk2(h[0][2], h[0][3]); o0.z = pk2(h[1][0], h[1][1]); o0.w = pk2(h[1][2], h[1][3]);
;                 o1.x = pk2(h[2][0], h[2][1]); o1.y = pk2(h[2][2], h[2][3]); o1.z = pk2(h[3][0], h[3][1]); o1.w = pk2(h[3][2], h[3][3]);
;                 v4u* hp = (v4u*)(hout + (size_t)m * D); hp[lane] = o0; hp[64 + lane] = o1;
; #pragma unroll
;                 for (int i = 0; i < 4; ++i) h[i] = h[i] * rh * q4[i];
;                 o0.x = pk2(h[0][0], h[0][1]); o0.y = pk2(h[0][2], h[0][3]); o0.z = pk2(h[1][0], h[1][1]); o0.w = pk2(h[1][2], h[1][3]);
;                 o1.x = pk2(h[2][0], h[2][1]); o1.y = pk2(h[2][2], h[2][3]); o1.z = pk2(h[3][0], h[3][1]); o1.w = pk2(h[3][2], h[3][3]);
;                 v4u* up = (v4u*)(u + (size_t)m * D); up[lane] = o0; up[64 + lane] = o1;
	v_pk_mul_f32 v[118:119], v[86:87], v[86:87]
	v_pk_mul_f32 v[120:121], v[84:85], v[84:85]
	v_mul_f32_e32 v2, v92, v92
	v_pk_mov_b32 v[122:123], v[120:121], v[118:119] op_sel:[1,0]
	v_mov_b32_e32 v121, v119
	v_pk_add_f32 v[118:119], v[122:123], v[120:121]
	v_pk_mul_f32 v[120:121], v[90:91], v[90:91]
	v_pk_mul_f32 v[122:123], v[88:89], v[88:89]
	v_pk_add_f32 v[118:119], v[118:119], v[118:119] op_sel_hi:[0,1]
	v_pk_mov_b32 v[124:125], v[122:123], v[120:121] op_sel:[1,0]
	v_mov_b32_e32 v123, v121
	v_pk_add_f32 v[120:121], v[124:125], v[122:123]
	v_pk_fma_f32 v[122:123], v[92:93], v[92:93], v[2:3] op_sel_hi:[1,1,0]
	v_mul_f32_e32 v2, v94, v94
	v_pk_add_f32 v[120:121], v[120:121], v[120:121] op_sel_hi:[0,1]
	v_pk_fma_f32 v[124:125], v[94:95], v[94:95], v[2:3] op_sel_hi:[1,1,0]
	v_mul_f32_e32 v122, v96, v96
	v_mul_f32_e32 v124, v97, v97
	v_mul_f32_e32 v118, v98, v98
	v_mul_f32_e32 v120, v99, v99
	v_pk_add_f32 v[122:123], v[122:123], v[124:125]
	v_pk_add_f32 v[118:119], v[118:119], v[120:121]
	v_cvt_pk_bf16_f32 v124, v96, v97
	v_cvt_pk_bf16_f32 v125, v98, v99
	s_nop 0
	v_pk_add_f32 v[118:119], v[122:123], v[118:119]
	v_cvt_pk_bf16_f32 v123, v94, v95
	s_nop 0
	v_add_f32_e32 v2, v118, v119
	s_nop 1
	v_add_f32_dpp v2, v2, v2 quad_perm:[1,0,3,2] row_mask:0xf bank_mask:0xf bound_ctrl:1
	s_nop 1
	v_add_f32_dpp v2, v2, v2 quad_perm:[2,3,0,1] row_mask:0xf bank_mask:0xf bound_ctrl:1
	s_nop 1
	v_add_f32_dpp v2, v2, v2 row_half_mirror row_mask:0xf bank_mask:0xf bound_ctrl:1
	s_nop 1
	v_add_f32_dpp v2, v2, v2 row_mirror row_mask:0xf bank_mask:0xf bound_ctrl:1
	s_nop 0
	v_readlane_b32 s1, v2, 16
	v_readlane_b32 s9, v2, 48
	v_readlane_b32 s4, v2, 0
	v_readlane_b32 s5, v2, 32
	v_mov_b32_e32 v118, s1
	v_mov_b32_e32 v119, s9
	v_pk_add_f32 v[118:119], s[4:5], v[118:119]
	s_brev_b32 s1, 64
	v_add_f32_e32 v2, v118, v119
	v_fmamk_f32 v2, v2, 0x3a800000, v214
	s_mov_b64 s[4:5], 0
	v_add_co_u32_e32 v126, vcc, s1, v116
	v_rsq_f32_e32 v2, v2
	s_nop 0
	v_cvt_pk_bf16_f32 v118, v84, v85
	v_cvt_pk_bf16_f32 v119, v86, v87
	v_cvt_pk_bf16_f32 v120, v88, v89
	v_cvt_pk_bf16_f32 v121, v90, v91
	v_cvt_pk_bf16_f32 v122, v92, v93
	s_nop 0
	v_addc_co_u32_e32 v127, vcc, 0, v117, vcc
	global_store_dwordx4 v[126:127], v[118:121], off sc1 nt
	global_store_dwordx4 v[126:127], v[122:125], off offset:1024 sc1 nt
	v_pk_mul_f32 v[126:127], v[92:93], v[2:3] op_sel_hi:[1,0]
	v_pk_mul_f32 v[118:119], v[84:85], v[2:3] op_sel_hi:[1,0]
	v_pk_mul_f32 v[120:121], v[86:87], v[2:3] op_sel_hi:[1,0]
	v_pk_mul_f32 v[122:123], v[88:89], v[2:3] op_sel_hi:[1,0]
	v_pk_mul_f32 v[120:121], v[26:27], v[120:121]
	v_pk_mul_f32 v[118:119], v[24:25], v[118:119]
	v_pk_mul_f32 v[122:123], v[20:21], v[122:123]
	v_pk_mul_f32 v[126:127], v[32:33], v[126:127]
	v_pk_mul_f32 v[124:125], v[90:91], v[2:3] op_sel_hi:[1,0]
	v_cvt_pk_bf16_f32 v118, v118, v119
	v_cvt_pk_bf16_f32 v119, v120, v121
	v_cvt_pk_bf16_f32 v120, v122, v123
	v_cvt_pk_bf16_f32 v122, v126, v127
	v_add_co_u32_e32 v126, vcc, 0xb000000, v114
	v_pk_mul_f32 v[124:125], v[22:23], v[124:125]
	v_pk_mul_f32 v[128:129], v[94:95], v[2:3] op_sel_hi:[1,0]
	v_pk_mul_f32 v[130:131], v[96:97], v[2:3] op_sel_hi:[1,0]
	v_pk_mul_f32 v[132:133], v[98:99], v[2:3] op_sel_hi:[1,0]
	v_cvt_pk_bf16_f32 v121, v124, v125
	v_addc_co_u32_e32 v127, vcc, 0, v115, vcc
	v_pk_mul_f32 v[128:129], v[34:35], v[128:129]
	v_pk_mul_f32 v[132:133], v[30:31], v[132:133]
	v_pk_mul_f32 v[130:131], v[28:29], v[130:131]
	v_cvt_pk_bf16_f32 v123, v128, v129
	v_cvt_pk_bf16_f32 v125, v132, v133
	s_nop 0
	v_cvt_pk_bf16_f32 v124, v130, v131
	flat_store_dwordx4 v[126:127], v[118:121] sc1
	flat_store_dwordx4 v[126:127], v[122:125] offset:1024 sc1
.LBB0_736:
	s_andn2_b64 vcc, exec, s[4:5]
	s_cbranch_vccnz .LBB0_738
	v_add_co_u32_e32 v118, vcc, 0xffffe000, v112
	s_nop 1
	v_addc_co_u32_e32 v119, vcc, -1, v113, vcc
	global_store_dwordx4 v[118:119], v[84:87], off offset:-2064 sc1 nt
	global_store_dwordx4 v[118:119], v[88:91], off offset:-2048 sc1 nt
	global_store_dwordx4 v[118:119], v[92:95], off offset:-16 sc1 nt
	global_store_dwordx4 v[118:119], v[96:99], off sc1 nt
.LBB0_738:
	s_nop 0
	v_lshlrev_b32_e32 v92, 16, v76
	v_and_b32_e32 v93, 0xffff0000, v76
	v_mul_f32_e32 v2, v92, v92
	v_lshlrev_b32_e32 v76, 16, v77
	v_pk_fma_f32 v[94:95], v[92:93], v[92:93], v[2:3] op_sel_hi:[1,1,0]
	v_and_b32_e32 v77, 0xffff0000, v77
	v_mul_f32_e32 v2, v76, v76
	v_lshlrev_b32_e32 v99, 16, v79
	v_lshlrev_b32_e32 v98, 16, v78
	v_and_b32_e32 v79, 0xffff0000, v79
	v_and_b32_e32 v78, 0xffff0000, v78
	v_lshlrev_b32_e32 v120, 16, v72
	v_lshlrev_b32_e32 v84, 16, v74
	v_pk_fma_f32 v[96:97], v[76:77], v[76:77], v[2:3] op_sel_hi:[1,1,0]
	v_pk_mul_f32 v[118:119], v[78:79], v[78:79]
	v_and_b32_e32 v121, 0xffff0000, v72
	v_mul_f32_e32 v2, v120, v120
	v_lshlrev_b32_e32 v124, 16, v73
	v_pk_fma_f32 v[118:119], v[98:99], v[98:99], v[118:119]
	v_pk_fma_f32 v[122:123], v[120:121], v[120:121], v[2:3] op_sel_hi:[1,1,0]
	v_and_b32_e32 v125, 0xffff0000, v73
	v_mul_f32_e32 v2, v124, v124
	v_mov_b32_e32 v85, v95
	v_mov_b32_e32 v126, v84
	v_mov_b32_e32 v127, v97
	v_and_b32_e32 v128, 0xffff0000, v74
	v_lshlrev_b32_e32 v86, 16, v75
	v_and_b32_e32 v87, 0xffff0000, v75
	v_pk_add_f32 v[118:119], v[118:119], v[118:119] op_sel_hi:[0,1]
	v_pk_fma_f32 v[72:73], v[124:125], v[124:125], v[2:3] op_sel_hi:[1,1,0]
	v_pk_mul_f32 v[126:127], v[84:85], v[126:127]
	v_pk_add_f32 v[94:95], v[94:95], v[96:97]
	v_mul_f32_e32 v118, v128, v128
	v_mul_f32_e32 v122, v86, v86
	v_mul_f32_e32 v72, v87, v87
	v_mov_b32_e32 v127, v95
	v_pk_add_f32 v[94:95], v[126:127], v[118:119]
	v_pk_add_f32 v[72:73], v[122:123], v[72:73]
	v_lshlrev_b32_e32 v90, 16, v68
	v_pk_add_f32 v[72:73], v[94:95], v[72:73]
; __device__ __forceinline__ void thin_pass(const Ctx& C, const bf16* hin, bf16* hout, bf16* u, float* out, const bf16* y, const float* gpost, float cmul, const float* gpre, bool last) {
;     ...
;             const int m = m0 + b; const v4u y0 = yr[b][0], y1 = yr[b][1], h0 = hr[b][0], h1 = hr[b][1];
;             f32x4 yv[4], h[4];
;             yv[0] = (f32x4){bf_lo(y0.x), bf_hi(y0.x), bf_lo(y0.y), bf_hi(y0.y)}; yv[1] = (f32x4){bf_lo(y0.z), bf_hi(y0.z), bf_lo(y0.w), bf_hi(y0.w)};
;             yv[2] = (f32x4){bf_lo(y1.x), bf_hi(y1.x), bf_lo(y1.y), bf_hi(y1.y)}; yv[3] = (f32x4){bf_lo(y1.z), bf_hi(y1.z), bf_lo(y1.w), bf_hi(y1.w)};
;             h[0] = (f32x4){bf_lo(h0.x), bf_hi(h0.x), bf_lo(h0.y), bf_hi(h0.y)}; h[1] = (f32x4){bf_lo(h0.z), bf_hi(h0.z), bf_lo(h0.w), bf_hi(h0.w)};
;             h[2] = (f32x4){bf_lo(h1.x), bf_hi(h1.x), bf_lo(h1.y), bf_hi(h1.y)}; h[3] = (f32x4){bf_lo(h1.z), bf_hi(h1.z), bf_lo(h1.w), bf_hi(h1.w)};
;             float ss = 0.f;
; #pragma unroll
;             for (int i = 0; i < 4; ++i) ss += (yv[i][0] * yv[i][0] + yv[i][1] * yv[i][1]) + (yv[i][2] * yv[i][2] + yv[i][3] * yv[i][3]);
;             const float ry = cmul / sqrtf(wave_sum(ss) * (1.0f / D) + RMS_EPS);
; #pragma unroll
;             for (int i = 0; i < 4; ++i) h[i] = h[i] + yv[i] * ry * g4[i];
;             if (last) { f32x4* op = (f32x4*)(out + (size_t)m * D); op[2 * lane] = h[0]; op[2 * lane + 1] = h[1]; op[128 + 2 * lane] = h[2]; op[128 + 2 * lane + 1] = h[3]; }
;             else {
;                 float s2 = 0.f;
; #pragma unroll
;                 for (int i = 0; i < 4; ++i) s2 += (h[i][0] * h[i][0] + h[i][1] * h[i][1]) + (h[i][2] * h[i][2] + h[i][3] * h[i][3]);
;                 const float rh = 1.0f / sqrtf(wave_sum(s2) * (1.0f / D) + RMS_EPS);
;                 v4u o0, o1; o0.x = pk2(h[0][0], h[0][1]); o0.y = pk2(h[0][2], h[0][3]); o0.z = pk2(h[1][0], h[1][1]); o0.w = pk2(h[1][2], h[1][3]);
;                 o1.x = pk2(h[2][0], h[2][1]); o1.y = pk2(h[2][2], h[2][3]); o1.z = pk2(h[3][0], h[3][1]); o1.w = pk2(h[3][2], h[3][3]);
;                 v4u* hp = (v4u*)(hout + (size_t)m * D); hp[lane] = o0; hp[64 + lane] = o1;
; #pragma unroll
;                 for (int i = 0; i < 4; ++i) h[i] = h[i] * rh * q4[i];
;                 o0.x = pk2(h[0][0], h[0][1]); o0.y = pk2(h[0][2], h[0][3]); o0.z = pk2(h[1][0], h[1][1]); o0.w = pk2(h[1][2], h[1][3]);
	v_and_b32_e32 v91, 0xffff0000, v68
	v_add_f32_e32 v2, v72, v73
	v_lshlrev_b32_e32 v94, 16, v69
	v_and_b32_e32 v95, 0xffff0000, v69
	v_add_f32_dpp v2, v2, v2 quad_perm:[1,0,3,2] row_mask:0xf bank_mask:0xf bound_ctrl:1
	v_lshlrev_b32_e32 v96, 16, v70
	v_and_b32_e32 v97, 0xffff0000, v70
	v_add_f32_dpp v2, v2, v2 quad_perm:[2,3,0,1] row_mask:0xf bank_mask:0xf bound_ctrl:1
	v_lshlrev_b32_e32 v118, 16, v71
	v_and_b32_e32 v119, 0xffff0000, v71
	v_add_f32_dpp v2, v2, v2 row_half_mirror row_mask:0xf bank_mask:0xf bound_ctrl:1
	v_lshlrev_b32_e32 v74, 16, v80
	v_and_b32_e32 v75, 0xffff0000, v80
	v_add_f32_dpp v2, v2, v2 row_mirror row_mask:0xf bank_mask:0xf bound_ctrl:1
	v_lshlrev_b32_e32 v80, 16, v81
	v_readlane_b32 s1, v2, 16
	v_readlane_b32 s9, v2, 48
	v_readlane_b32 s4, v2, 0
	v_readlane_b32 s5, v2, 32
	v_mov_b32_e32 v72, s1
	v_mov_b32_e32 v73, s9
	v_pk_add_f32 v[72:73], s[4:5], v[72:73]
	v_and_b32_e32 v81, 0xffff0000, v81
	v_add_f32_e32 v2, v72, v73
	v_fmamk_f32 v2, v2, 0x3a800000, v214
	v_mov_b32_e32 v73, v78
	v_mov_b32_e32 v78, v99
	v_lshlrev_b32_e32 v88, 16, v82
	v_and_b32_e32 v89, 0xffff0000, v82
	v_lshlrev_b32_e32 v82, 16, v83
	v_and_b32_e32 v83, 0xffff0000, v83
	v_mov_b32_e32 v85, v128
	s_mov_b64 s[4:5], -1
	v_rsq_f32_e32 v2, v2
	s_nop 0
	v_mul_f32_e32 v2, 0.5, v2
	v_pk_mul_f32 v[68:69], v[2:3], v[92:93] op_sel_hi:[0,1]
	v_pk_mul_f32 v[70:71], v[2:3], v[76:77] op_sel_hi:[0,1]
	v_pk_fma_f32 v[68:69], v[8:9], v[68:69], v[74:75]
	v_mov_b32_e32 v72, v98
	v_pk_mul_f32 v[74:75], v[2:3], v[78:79] op_sel_hi:[0,1]
	v_pk_fma_f32 v[70:71], v[10:11], v[70:71], v[80:81]
	v_pk_mul_f32 v[72:73], v[2:3], v[72:73] op_sel_hi:[0,1]
	v_pk_fma_f32 v[74:75], v[6:7], v[74:75], v[82:83]
	v_pk_mul_f32 v[76:77], v[2:3], v[120:121] op_sel_hi:[0,1]
	v_pk_mul_f32 v[78:79], v[2:3], v[124:125] op_sel_hi:[0,1]
	v_pk_mul_f32 v[80:81], v[84:85], v[2:3] op_sel_hi:[1,0]
	v_pk_mul_f32 v[82:83], v[86:87], v[2:3] op_sel_hi:[1,0]
	v_pk_fma_f32 v[72:73], v[4:5], v[72:73], v[88:89]
	v_pk_fma_f32 v[78:79], v[18:19], v[78:79], v[94:95]
	v_pk_fma_f32 v[76:77], v[16:17], v[76:77], v[90:91]
	v_pk_fma_f32 v[82:83], v[14:15], v[82:83], v[118:119]
	v_pk_fma_f32 v[80:81], v[12:13], v[80:81], v[96:97]
	s_and_b64 vcc, exec, s[2:3]
	s_cbranch_vccnz .LBB0_740
	v_pk_mul_f32 v[84:85], v[70:71], v[70:71]
	v_pk_mul_f32 v[86:87], v[68:69], v[68:69]
	v_mul_f32_e32 v2, v76, v76
	v_pk_mov_b32 v[88:89], v[86:87], v[84:85] op_sel:[1,0]
	v_mov_b32_e32 v87, v85
	v_pk_add_f32 v[84:85], v[88:89], v[86:87]
	v_pk_mul_f32 v[86:87], v[74:75], v[74:75]
	v_pk_mul_f32 v[88:89], v[72:73], v[72:73]
	v_pk_add_f32 v[84:85], v[84:85], v[84:85] op_sel_hi:[0,1]
	v_pk_mov_b32 v[90:91], v[88:89], v[86:87] op_sel:[1,0]
	v_mov_b32_e32 v89, v87
	v_pk_add_f32 v[86:87], v[90:91], v[88:89]
	v_pk_fma_f32 v[88:89], v[76:77], v[76:77], v[2:3] op_sel_hi:[1,1,0]
	v_mul_f32_e32 v2, v78, v78
	v_pk_add_f32 v[86:87], v[86:87], v[86:87] op_sel_hi:[0,1]
	v_pk_fma_f32 v[90:91], v[78:79], v[78:79], v[2:3] op_sel_hi:[1,1,0]
	v_mul_f32_e32 v88, v80, v80
	v_mul_f32_e32 v90, v81, v81
	v_mul_f32_e32 v84, v82, v82
	v_mul_f32_e32 v86, v83, v83
	v_pk_add_f32 v[88:89], v[88:89], v[90:91]
	v_pk_add_f32 v[84:85], v[84:85], v[86:87]
	v_cvt_pk_bf16_f32 v90, v80, v81
	v_cvt_pk_bf16_f32 v91, v82, v83
	s_nop 0
	v_pk_add_f32 v[84:85], v[88:89], v[84:85]
	v_cvt_pk_bf16_f32 v89, v78, v79
	s_nop 0
	v_add_f32_e32 v2, v84, v85
	s_nop 1
	v_add_f32_dpp v2, v2, v2 quad_perm:[1,0,3,2] row_mask:0xf bank_mask:0xf bound_ctrl:1
	s_nop 1
	v_add_f32_dpp v2, v2, v2 quad_perm:[2,3,0,1] row_mask:0xf bank_mask:0xf bound_ctrl:1
	s_nop 1
	v_add_f32_dpp v2, v2, v2 row_half_mirror row_mask:0xf bank_mask:0xf bound_ctrl:1
	s_nop 1
	v_add_f32_dpp v2, v2, v2 row_mirror row_mask:0xf bank_mask:0xf bound_ctrl:1
	s_nop 0
	v_readlane_b32 s1, v2, 16
	v_readlane_b32 s9, v2, 48
	v_readlane_b32 s4, v2, 0
	v_readlane_b32 s5, v2, 32
	v_mov_b32_e32 v84, s1
	v_mov_b32_e32 v85, s9
	v_pk_add_f32 v[84:85], s[4:5], v[84:85]
	s_brev_b32 s1, 64
	v_add_f32_e32 v2, v84, v85
	v_fmamk_f32 v2, v2, 0x3a800000, v214
	s_mov_b64 s[4:5], 0
	v_add_co_u32_e32 v92, vcc, s1, v116
	v_rsq_f32_e32 v2, v2
	s_nop 0
	v_cvt_pk_bf16_f32 v84, v68, v69
	v_cvt_pk_bf16_f32 v85, v70, v71
	v_cvt_pk_bf16_f32 v86, v72, v73
	v_cvt_pk_bf16_f32 v87, v74, v75
	v_cvt_pk_bf16_f32 v88, v76, v77
	s_nop 0
	v_addc_co_u32_e32 v93, vcc, 0, v117, vcc
	global_store_dwordx4 v[92:93], v[84:87], off offset:2048 sc1 nt
	global_store_dwordx4 v[92:93], v[88:91], off offset:3072 sc1 nt
	v_pk_mul_f32 v[92:93], v[76:77], v[2:3] op_sel_hi:[1,0]
	v_pk_mul_f32 v[84:85], v[68:69], v[2:3] op_sel_hi:[1,0]
	v_pk_mul_f32 v[86:87], v[70:71], v[2:3] op_sel_hi:[1,0]
	v_pk_mul_f32 v[88:89], v[72:73], v[2:3] op_sel_hi:[1,0]
	v_pk_mul_f32 v[86:87], v[26:27], v[86:87]
	v_pk_mul_f32 v[84:85], v[24:25], v[84:85]
	v_pk_mul_f32 v[88:89], v[20:21], v[88:89]
	v_pk_mul_f32 v[92:93], v[32:33], v[92:93]
	v_pk_mul_f32 v[90:91], v[74:75], v[2:3] op_sel_hi:[1,0]
	v_cvt_pk_bf16_f32 v84, v84, v85
	v_cvt_pk_bf16_f32 v85, v86, v87
	v_cvt_pk_bf16_f32 v86, v88, v89
	v_cvt_pk_bf16_f32 v88, v92, v93
	v_add_co_u32_e32 v92, vcc, 0xb000000, v114
	v_pk_mul_f32 v[90:91], v[22:23], v[90:91]
	v_pk_mul_f32 v[94:95], v[78:79], v[2:3] op_sel_hi:[1,0]
	v_pk_mul_f32 v[96:97], v[80:81], v[2:3] op_sel_hi:[1,0]
	v_pk_mul_f32 v[98:99], v[82:83], v[2:3] op_sel_hi:[1,0]
	v_cvt_pk_bf16_f32 v87, v90, v91
	v_addc_co_u32_e32 v93, vcc, 0, v115, vcc
	v_pk_mul_f32 v[94:95], v[34:35], v[94:95]
	v_pk_mul_f32 v[98:99], v[30:31], v[98:99]
	v_pk_mul_f32 v[96:97], v[28:29], v[96:97]
	v_cvt_pk_bf16_f32 v89, v94, v95
	v_cvt_pk_bf16_f32 v91, v98, v99
	s_nop 0
	v_cvt_pk_bf16_f32 v90, v96, v97
	flat_store_dwordx4 v[92:93], v[84:87] offset:2048 sc1
	flat_store_dwordx4 v[92:93], v[88:91] offset:3072 sc1
; __device__ __forceinline__ void thin_pass(const Ctx& C, const bf16* hin, bf16* hout, bf16* u, float* out, const bf16* y, const float* gpost, float cmul, const float* gpre, bool last) {
;     ...
;             const int m = m0 + b; const v4u y0 = yr[b][0], y1 = yr[b][1], h0 = hr[b][0], h1 = hr[b][1];
;             f32x4 yv[4], h[4];
;             yv[0] = (f32x4){bf_lo(y0.x), bf_hi(y0.x), bf_lo(y0.y), bf_hi(y0.y)}; yv[1] = (f32x4){bf_lo(y0.z), bf_hi(y0.z), bf_lo(y0.w), bf_hi(y0.w)};
;             yv[2] = (f32x4){bf_lo(y1.x), bf_hi(y1.x), bf_lo(y1.y), bf_hi(y1.y)}; yv[3] = (f32x4){bf_lo(y1.z), bf_hi(y1.z), bf_lo(y1.w), bf_hi(y1.w)};
;             h[0] = (f32x4){bf_lo(h0.x), bf_hi(h0.x), bf_lo(h0.y), bf_hi(h0.y)}; h[1] = (f32x4){bf_lo(h0.z), bf_hi(h0.z), bf_lo(h0.w), bf_hi(h0.w)};
;             h[2] = (f32x4){bf_lo(h1.x), bf_hi(h1.x), bf_lo(h1.y), bf_hi(h1.y)}; h[3] = (f32x4){bf_lo(h1.z), bf_hi(h1.z), bf_lo(h1.w), bf_hi(h1.w)};
;             float ss = 0.f;
; #pragma unroll
;             for (int i = 0; i < 4; ++i) ss += (yv[i][0] * yv[i][0] + yv[i][1] * yv[i][1]) + (yv[i][2] * yv[i][2] + yv[i][3] * yv[i][3]);
;             const float ry = cmul / sqrtf(wave_sum(ss) * (1.0f / D) + RMS_EPS);
; #pragma unroll
;             for (int i = 0; i < 4; ++i) h[i] = h[i] + yv[i] * ry * g4[i];
;             if (last) { f32x4* op = (f32x4*)(out + (size_t)m * D); op[2 * lane] = h[0]; op[2 * lane + 1] = h[1]; op[128 + 2 * lane] = h[2]; op[128 + 2 * lane + 1] = h[3]; }
.LBB0_740:
	s_andn2_b64 vcc, exec, s[4:5]
	s_cbranch_vccnz .LBB0_742
	v_add_co_u32_e32 v84, vcc, 0xfffff000, v112
	s_nop 1
	v_addc_co_u32_e32 v85, vcc, -1, v113, vcc
	global_store_dwordx4 v[84:85], v[68:71], off offset:-2064 sc1 nt
	global_store_dwordx4 v[84:85], v[72:75], off offset:-2048 sc1 nt
	global_store_dwordx4 v[84:85], v[76:79], off offset:-16 sc1 nt
	global_store_dwordx4 v[112:113], v[80:83], off offset:-4096 sc1 nt
.LBB0_742:
	s_nop 0
	v_lshlrev_b32_e32 v76, 16, v60
	v_and_b32_e32 v77, 0xffff0000, v60
	v_mul_f32_e32 v2, v76, v76
	v_lshlrev_b32_e32 v60, 16, v61
	v_pk_fma_f32 v[78:79], v[76:77], v[76:77], v[2:3] op_sel_hi:[1,1,0]
	v_and_b32_e32 v61, 0xffff0000, v61
	v_mul_f32_e32 v2, v60, v60
	v_lshlrev_b32_e32 v83, 16, v63
	v_lshlrev_b32_e32 v82, 16, v62
	v_and_b32_e32 v63, 0xffff0000, v63
	v_and_b32_e32 v62, 0xffff0000, v62
	v_lshlrev_b32_e32 v86, 16, v56
	v_lshlrev_b32_e32 v68, 16, v58
	v_pk_fma_f32 v[80:81], v[60:61], v[60:61], v[2:3] op_sel_hi:[1,1,0]
	v_pk_mul_f32 v[84:85], v[62:63], v[62:63]
	v_and_b32_e32 v87, 0xffff0000, v56
	v_mul_f32_e32 v2, v86, v86
	v_lshlrev_b32_e32 v90, 16, v57
	v_pk_fma_f32 v[84:85], v[82:83], v[82:83], v[84:85]
	v_pk_fma_f32 v[88:89], v[86:87], v[86:87], v[2:3] op_sel_hi:[1,1,0]
	v_and_b32_e32 v91, 0xffff0000, v57
	v_mul_f32_e32 v2, v90, v90
	v_mov_b32_e32 v69, v79
	v_mov_b32_e32 v92, v68
	v_mov_b32_e32 v93, v81
	v_and_b32_e32 v94, 0xffff0000, v58
	v_lshlrev_b32_e32 v70, 16, v59
	v_and_b32_e32 v71, 0xffff0000, v59
	v_pk_add_f32 v[84:85], v[84:85], v[84:85] op_sel_hi:[0,1]
	v_pk_fma_f32 v[56:57], v[90:91], v[90:91], v[2:3] op_sel_hi:[1,1,0]
	v_pk_mul_f32 v[92:93], v[68:69], v[92:93]
	v_pk_add_f32 v[78:79], v[78:79], v[80:81]
	v_mul_f32_e32 v84, v94, v94
	v_mul_f32_e32 v88, v70, v70
	v_mul_f32_e32 v56, v71, v71
	v_mov_b32_e32 v93, v79
	v_pk_add_f32 v[78:79], v[92:93], v[84:85]
	v_pk_add_f32 v[56:57], v[88:89], v[56:57]
	v_lshlrev_b32_e32 v74, 16, v52
	v_pk_add_f32 v[56:57], v[78:79], v[56:57]
	v_and_b32_e32 v75, 0xffff0000, v52
	v_add_f32_e32 v2, v56, v57
	v_lshlrev_b32_e32 v78, 16, v53
	v_and_b32_e32 v79, 0xffff0000, v53
	v_add_f32_dpp v2, v2, v2 quad_perm:[1,0,3,2] row_mask:0xf bank_mask:0xf bound_ctrl:1
	v_lshlrev_b32_e32 v80, 16, v54
	v_and_b32_e32 v81, 0xffff0000, v54
	v_add_f32_dpp v2, v2, v2 quad_perm:[2,3,0,1] row_mask:0xf bank_mask:0xf bound_ctrl:1
	v_lshlrev_b32_e32 v84, 16, v55
	v_and_b32_e32 v85, 0xffff0000, v55
	v_add_f32_dpp v2, v2, v2 row_half_mirror row_mask:0xf bank_mask:0xf bound_ctrl:1
	v_lshlrev_b32_e32 v58, 16, v64
	v_and_b32_e32 v59, 0xffff0000, v64
	v_add_f32_dpp v2, v2, v2 row_mirror row_mask:0xf bank_mask:0xf bound_ctrl:1
	v_lshlrev_b32_e32 v64, 16, v65
	v_readlane_b32 s1, v2, 16
	v_readlane_b32 s9, v2, 48
	v_readlane_b32 s4, v2, 0
	v_readlane_b32 s5, v2, 32
	v_mov_b32_e32 v56, s1
	v_mov_b32_e32 v57, s9
	v_pk_add_f32 v[56:57], s[4:5], v[56:57]
	v_and_b32_e32 v65, 0xffff0000, v65
	v_add_f32_e32 v2, v56, v57
	v_fmamk_f32 v2, v2, 0x3a800000, v214
	v_mov_b32_e32 v57, v62
	v_mov_b32_e32 v62, v83
	v_lshlrev_b32_e32 v72, 16, v66
	v_and_b32_e32 v73, 0xffff0000, v66
	v_lshlrev_b32_e32 v66, 16, v67
	v_and_b32_e32 v67, 0xffff0000, v67
	v_mov_b32_e32 v69, v94
	s_mov_b64 s[4:5], -1
	v_rsq_f32_e32 v2, v2
	s_nop 0
	v_mul_f32_e32 v2, 0.5, v2
	v_pk_mul_f32 v[52:53], v[2:3], v[76:77] op_sel_hi:[0,1]
	v_pk_mul_f32 v[54:55], v[2:3], v[60:61] op_sel_hi:[0,1]
	v_pk_fma_f32 v[52:53], v[8:9], v[52:53], v[58:59]
	v_mov_b32_e32 v56, v82
	v_pk_mul_f32 v[58:59], v[2:3], v[62:63] op_sel_hi:[0,1]
	v_pk_fma_f32 v[54:55], v[10:11], v[54:55], v[64:65]
	v_pk_mul_f32 v[56:57], v[2:3], v[56:57] op_sel_hi:[0,1]
	v_pk_fma_f32 v[58:59], v[6:7], v[58:59], v[66:67]
	v_pk_mul_f32 v[60:61], v[2:3], v[86:87] op_sel_hi:[0,1]
	v_pk_mul_f32 v[62:63], v[2:3], v[90:91] op_sel_hi:[0,1]
	v_pk_mul_f32 v[64:65], v[68:69], v[2:3] op_sel_hi:[1,0]
	v_pk_mul_f32 v[66:67], v[70:71], v[2:3] op_sel_hi:[1,0]
	v_pk_fma_f32 v[56:57], v[4:5], v[56:57], v[72:73]
	v_pk_fma_f32 v[62:63], v[18:19], v[62:63], v[78:79]
	v_pk_fma_f32 v[60:61], v[16:17], v[60:61], v[74:75]
	v_pk_fma_f32 v[66:67], v[14:15], v[66:67], v[84:85]
	v_pk_fma_f32 v[64:65], v[12:13], v[64:65], v[80:81]
	s_and_b64 vcc, exec, s[2:3]
	s_cbranch_vccnz .LBB0_744
	v_pk_mul_f32 v[68:69], v[54:55], v[54:55]
	v_pk_mul_f32 v[70:71], v[52:53], v[52:53]
	v_mul_f32_e32 v2, v60, v60
	v_pk_mov_b32 v[72:73], v[70:71], v[68:69] op_sel:[1,0]
	v_mov_b32_e32 v71, v69
	v_pk_add_f32 v[68:69], v[72:73], v[70:71]
	v_pk_mul_f32 v[70:71], v[58:59], v[58:59]
	v_pk_mul_f32 v[72:73], v[56:57], v[56:57]
	v_pk_add_f32 v[68:69], v[68:69], v[68:69] op_sel_hi:[0,1]
	v_pk_mov_b32 v[74:75], v[72:73], v[70:71] op_sel:[1,0]
	v_mov_b32_e32 v73, v71
	v_pk_add_f32 v[70:71], v[74:75], v[72:73]
	v_pk_fma_f32 v[72:73], v[60:61], v[60:61], v[2:3] op_sel_hi:[1,1,0]
	v_mul_f32_e32 v2, v62, v62
	v_pk_add_f32 v[70:71], v[70:71], v[70:71] op_sel_hi:[0,1]
	v_pk_fma_f32 v[74:75], v[62:63], v[62:63], v[2:3] op_sel_hi:[1,1,0]
	v_mul_f32_e32 v72, v64, v64
	v_mul_f32_e32 v74, v65, v65
	v_mul_f32_e32 v68, v66, v66
	v_mul_f32_e32 v70, v67, v67
	v_pk_add_f32 v[72:73], v[72:73], v[74:75]
	v_pk_add_f32 v[68:69], v[68:69], v[70:71]
	v_cvt_pk_bf16_f32 v74, v64, v65
	v_cvt_pk_bf16_f32 v75, v66, v67
	s_nop 0
	v_pk_add_f32 v[68:69], v[72:73], v[68:69]
	v_cvt_pk_bf16_f32 v73, v62, v63
	s_nop 0
	v_add_f32_e32 v2, v68, v69
	s_nop 1
	v_add_f32_dpp v2, v2, v2 quad_perm:[1,0,3,2] row_mask:0xf bank_mask:0xf bound_ctrl:1
	s_nop 1
	v_add_f32_dpp v2, v2, v2 quad_perm:[2,3,0,1] row_mask:0xf bank_mask:0xf bound_ctrl:1
	s_nop 1
	v_add_f32_dpp v2, v2, v2 row_half_mirror row_mask:0xf bank_mask:0xf bound_ctrl:1
	s_nop 1
; __device__ __forceinline__ void thin_pass(const Ctx& C, const bf16* hin, bf16* hout, bf16* u, float* out, const bf16* y, const float* gpost, float cmul, const float* gpre, bool last) {
;     ...
;             const int m = m0 + b; const v4u y0 = yr[b][0], y1 = yr[b][1], h0 = hr[b][0], h1 = hr[b][1];
;             f32x4 yv[4], h[4];
;             yv[0] = (f32x4){bf_lo(y0.x), bf_hi(y0.x), bf_lo(y0.y), bf_hi(y0.y)}; yv[1] = (f32x4){bf_lo(y0.z), bf_hi(y0.z), bf_lo(y0.w), bf_hi(y0.w)};
;             yv[2] = (f32x4){bf_lo(y1.x), bf_hi(y1.x), bf_lo(y1.y), bf_hi(y1.y)}; yv[3] = (f32x4){bf_lo(y1.z), bf_hi(y1.z), bf_lo(y1.w), bf_hi(y1.w)};
;             h[0] = (f32x4){bf_lo(h0.x), bf_hi(h0.x), bf_lo(h0.y), bf_hi(h0.y)}; h[1] = (f32x4){bf_lo(h0.z), bf_hi(h0.z), bf_lo(h0.w), bf_hi(h0.w)};
;             h[2] = (f32x4){bf_lo(h1.x), bf_hi(h1.x), bf_lo(h1.y), bf_hi(h1.y)}; h[3] = (f32x4){bf_lo(h1.z), bf_hi(h1.z), bf_lo(h1.w), bf_hi(h1.w)};
;             float ss = 0.f;
; #pragma unroll
;     ...
;             if (last) { f32x4* op = (f32x4*)(out + (size_t)m * D); op[2 * lane] = h[0]; op[2 * lane + 1] = h[1]; op[128 + 2 * lane] = h[2]; op[128 + 2 * lane + 1] = h[3]; }
;             else {
;                 float s2 = 0.f;
; #pragma unroll
;                 for (int i = 0; i < 4; ++i) s2 += (h[i][0] * h[i][0] + h[i][1] * h[i][1]) + (h[i][2] * h[i][2] + h[i][3] * h[i][3]);
;                 const float rh = 1.0f / sqrtf(wave_sum(s2) * (1.0f / D) + RMS_EPS);
;                 v4u o0, o1; o0.x = pk2(h[0][0], h[0][1]); o0.y = pk2(h[0][2], h[0][3]); o0.z = pk2(h[1][0], h[1][1]); o0.w = pk2(h[1][2], h[1][3]);
;                 o1.x = pk2(h[2][0], h[2][1]); o1.y = pk2(h[2][2], h[2][3]); o1.z = pk2(h[3][0], h[3][1]); o1.w = pk2(h[3][2], h[3][3]);
;                 v4u* hp = (v4u*)(hout + (size_t)m * D); hp[lane] = o0; hp[64 + lane] = o1;
; #pragma unroll
;                 for (int i = 0; i < 4; ++i) h[i] = h[i] * rh * q4[i];
;                 o0.x = pk2(h[0][0], h[0][1]); o0.y = pk2(h[0][2], h[0][3]); o0.z = pk2(h[1][0], h[1][1]); o0.w = pk2(h[1][2], h[1][3]);
;                 o1.x = pk2(h[2][0], h[2][1]); o1.y = pk2(h[2][2], h[2][3]); o1.z = pk2(h[3][0], h[3][1]); o1.w = pk2(h[3][2], h[3][3]);
;                 v4u* up = (v4u*)(u + (size_t)m * D); up[lane] = o0; up[64 + lane] = o1;
	v_add_f32_dpp v2, v2, v2 row_mirror row_mask:0xf bank_mask:0xf bound_ctrl:1
	s_nop 0
	v_readlane_b32 s1, v2, 16
	v_readlane_b32 s9, v2, 48
	v_readlane_b32 s4, v2, 0
	v_readlane_b32 s5, v2, 32
	v_mov_b32_e32 v68, s1
	v_mov_b32_e32 v69, s9
	v_pk_add_f32 v[68:69], s[4:5], v[68:69]
	s_nop 0
	v_add_f32_e32 v2, v68, v69
	v_fmamk_f32 v2, v2, 0x3a800000, v214
	s_mov_b64 s[4:5], 0
	v_add_co_u32_e32 v76, vcc, s93, v116
	v_rsq_f32_e32 v2, v2
	s_nop 0
	v_cvt_pk_bf16_f32 v68, v52, v53
	v_cvt_pk_bf16_f32 v69, v54, v55
	v_cvt_pk_bf16_f32 v70, v56, v57
	v_cvt_pk_bf16_f32 v71, v58, v59
	v_cvt_pk_bf16_f32 v72, v60, v61
	s_nop 0
	v_addc_co_u32_e32 v77, vcc, 0, v117, vcc
	global_store_dwordx4 v[76:77], v[68:71], off sc1 nt
	global_store_dwordx4 v[76:77], v[72:75], off offset:1024 sc1 nt
	v_pk_mul_f32 v[76:77], v[60:61], v[2:3] op_sel_hi:[1,0]
	v_pk_mul_f32 v[68:69], v[52:53], v[2:3] op_sel_hi:[1,0]
	v_pk_mul_f32 v[70:71], v[54:55], v[2:3] op_sel_hi:[1,0]
	v_pk_mul_f32 v[72:73], v[56:57], v[2:3] op_sel_hi:[1,0]
	v_pk_mul_f32 v[70:71], v[26:27], v[70:71]
	v_pk_mul_f32 v[68:69], v[24:25], v[68:69]
	v_pk_mul_f32 v[72:73], v[20:21], v[72:73]
	v_pk_mul_f32 v[76:77], v[32:33], v[76:77]
	v_pk_mul_f32 v[74:75], v[58:59], v[2:3] op_sel_hi:[1,0]
	v_cvt_pk_bf16_f32 v68, v68, v69
	v_cvt_pk_bf16_f32 v69, v70, v71
	v_cvt_pk_bf16_f32 v70, v72, v73
	v_cvt_pk_bf16_f32 v72, v76, v77
	v_add_co_u32_e32 v76, vcc, 0xb001000, v114
	v_pk_mul_f32 v[74:75], v[22:23], v[74:75]
	v_pk_mul_f32 v[78:79], v[62:63], v[2:3] op_sel_hi:[1,0]
	v_pk_mul_f32 v[80:81], v[64:65], v[2:3] op_sel_hi:[1,0]
	v_pk_mul_f32 v[82:83], v[66:67], v[2:3] op_sel_hi:[1,0]
	v_cvt_pk_bf16_f32 v71, v74, v75
	v_addc_co_u32_e32 v77, vcc, 0, v115, vcc
	v_pk_mul_f32 v[78:79], v[34:35], v[78:79]
	v_pk_mul_f32 v[82:83], v[30:31], v[82:83]
	v_pk_mul_f32 v[80:81], v[28:29], v[80:81]
	v_cvt_pk_bf16_f32 v73, v78, v79
	v_cvt_pk_bf16_f32 v75, v82, v83
	s_nop 0
	v_cvt_pk_bf16_f32 v74, v80, v81
	flat_store_dwordx4 v[76:77], v[68:71] sc1
	flat_store_dwordx4 v[76:77], v[72:75] offset:1024 sc1
.LBB0_744:
	s_andn2_b64 vcc, exec, s[4:5]
	s_cbranch_vccnz .LBB0_746
	global_store_dwordx4 v[112:113], v[52:55], off offset:-2064 sc1 nt
	global_store_dwordx4 v[112:113], v[56:59], off offset:-2048 sc1 nt
	global_store_dwordx4 v[112:113], v[60:63], off offset:-16 sc1 nt
	global_store_dwordx4 v[112:113], v[64:67], off sc1 nt
.LBB0_746:
	s_nop 0
	v_lshlrev_b32_e32 v60, 16, v44
	v_and_b32_e32 v61, 0xffff0000, v44
	v_mul_f32_e32 v2, v60, v60
	v_lshlrev_b32_e32 v44, 16, v45
	v_pk_fma_f32 v[62:63], v[60:61], v[60:61], v[2:3] op_sel_hi:[1,1,0]
	v_and_b32_e32 v45, 0xffff0000, v45
	v_mul_f32_e32 v2, v44, v44
	v_lshlrev_b32_e32 v67, 16, v47
	v_lshlrev_b32_e32 v66, 16, v46
	v_and_b32_e32 v47, 0xffff0000, v47
	v_and_b32_e32 v46, 0xffff0000, v46
	v_lshlrev_b32_e32 v70, 16, v40
	v_lshlrev_b32_e32 v52, 16, v42
	v_pk_fma_f32 v[64:65], v[44:45], v[44:45], v[2:3] op_sel_hi:[1,1,0]
	v_pk_mul_f32 v[68:69], v[46:47], v[46:47]
	v_and_b32_e32 v71, 0xffff0000, v40
	v_mul_f32_e32 v2, v70, v70
	v_lshlrev_b32_e32 v74, 16, v41
	v_pk_fma_f32 v[68:69], v[66:67], v[66:67], v[68:69]
	v_pk_fma_f32 v[72:73], v[70:71], v[70:71], v[2:3] op_sel_hi:[1,1,0]
	v_and_b32_e32 v75, 0xffff0000, v41
	v_mul_f32_e32 v2, v74, v74
	v_mov_b32_e32 v53, v63
	v_mov_b32_e32 v76, v52
	v_mov_b32_e32 v77, v65
	v_and_b32_e32 v78, 0xffff0000, v42
	v_lshlrev_b32_e32 v54, 16, v43
	v_and_b32_e32 v55, 0xffff0000, v43
	v_pk_add_f32 v[68:69], v[68:69], v[68:69] op_sel_hi:[0,1]
	v_pk_fma_f32 v[40:41], v[74:75], v[74:75], v[2:3] op_sel_hi:[1,1,0]
	v_pk_mul_f32 v[76:77], v[52:53], v[76:77]
	v_pk_add_f32 v[62:63], v[62:63], v[64:65]
	v_mul_f32_e32 v68, v78, v78
	v_mul_f32_e32 v72, v54, v54
	v_mul_f32_e32 v40, v55, v55
	v_mov_b32_e32 v77, v63
	v_pk_add_f32 v[62:63], v[76:77], v[68:69]
	v_pk_add_f32 v[40:41], v[72:73], v[40:41]
	v_lshlrev_b32_e32 v58, 16, v36
	v_pk_add_f32 v[40:41], v[62:63], v[40:41]
	v_and_b32_e32 v59, 0xffff0000, v36
	v_add_f32_e32 v2, v40, v41
	v_lshlrev_b32_e32 v62, 16, v37
	v_and_b32_e32 v63, 0xffff0000, v37
	v_add_f32_dpp v2, v2, v2 quad_perm:[1,0,3,2] row_mask:0xf bank_mask:0xf bound_ctrl:1
	v_lshlrev_b32_e32 v64, 16, v38
	v_and_b32_e32 v65, 0xffff0000, v38
	v_add_f32_dpp v2, v2, v2 quad_perm:[2,3,0,1] row_mask:0xf bank_mask:0xf bound_ctrl:1
	v_lshlrev_b32_e32 v68, 16, v39
	v_and_b32_e32 v69, 0xffff0000, v39
	v_add_f32_dpp v2, v2, v2 row_half_mirror row_mask:0xf bank_mask:0xf bound_ctrl:1
	v_lshlrev_b32_e32 v42, 16, v48
	v_and_b32_e32 v43, 0xffff0000, v48
	v_add_f32_dpp v2, v2, v2 row_mirror row_mask:0xf bank_mask:0xf bound_ctrl:1
	v_lshlrev_b32_e32 v48, 16, v49
	v_readlane_b32 s1, v2, 16
	v_readlane_b32 s9, v2, 48
	v_readlane_b32 s4, v2, 0
	v_readlane_b32 s5, v2, 32
	v_mov_b32_e32 v40, s1
	v_mov_b32_e32 v41, s9
	v_pk_add_f32 v[40:41], s[4:5], v[40:41]
	v_and_b32_e32 v49, 0xffff0000, v49
	v_add_f32_e32 v2, v40, v41
	v_fmamk_f32 v2, v2, 0x3a800000, v214
	v_mov_b32_e32 v41, v46
	v_mov_b32_e32 v46, v67
	v_lshlrev_b32_e32 v56, 16, v50
	v_and_b32_e32 v57, 0xffff0000, v50
	v_lshlrev_b32_e32 v50, 16, v51
	v_and_b32_e32 v51, 0xffff0000, v51
	v_mov_b32_e32 v53, v78
	v_rsq_f32_e32 v2, v2
	s_nop 0
	v_mul_f32_e32 v2, 0.5, v2
	v_pk_mul_f32 v[36:37], v[2:3], v[60:61] op_sel_hi:[0,1]
	v_pk_mul_f32 v[38:39], v[2:3], v[44:45] op_sel_hi:[0,1]
	v_pk_fma_f32 v[36:37], v[8:9], v[36:37], v[42:43]
	v_mov_b32_e32 v40, v66
	v_pk_mul_f32 v[42:43], v[2:3], v[46:47] op_sel_hi:[0,1]
	v_pk_fma_f32 v[38:39], v[10:11], v[38:39], v[48:49]
	v_pk_mul_f32 v[40:41], v[2:3], v[40:41] op_sel_hi:[0,1]
	v_pk_fma_f32 v[42:43], v[6:7], v[42:43], v[50:51]
	v_pk_mul_f32 v[44:45], v[2:3], v[70:71] op_sel_hi:[0,1]
	v_pk_mul_f32 v[46:47], v[2:3], v[74:75] op_sel_hi:[0,1]
	v_pk_mul_f32 v[48:49], v[52:53], v[2:3] op_sel_hi:[1,0]
	v_pk_mul_f32 v[50:51], v[54:55], v[2:3] op_sel_hi:[1,0]
	v_pk_fma_f32 v[40:41], v[4:5], v[40:41], v[56:57]
	v_pk_fma_f32 v[46:47], v[18:19], v[46:47], v[62:63]
	v_pk_fma_f32 v[44:45], v[16:17], v[44:45], v[58:59]
	v_pk_fma_f32 v[50:51], v[14:15], v[50:51], v[68:69]
	v_pk_fma_f32 v[48:49], v[12:13], v[48:49], v[64:65]
	s_and_b64 vcc, exec, s[2:3]
	s_mov_b64 s[2:3], -1
	s_cbranch_vccnz .LBB0_748
; __device__ __forceinline__ unsigned pk2(float lo, float hi) { unsigned r; asm("v_cvt_pk_bf16_f32 %0, %1, %2" : "=v"(r) : "v"(lo), "v"(hi)); return r; }
; __device__ __forceinline__ void thin_pass(const Ctx& C, const bf16* hin, bf16* hout, bf16* u, float* out, const bf16* y, const float* gpost, float cmul, const float* gpre, bool last) {
;     ...
;             if (last) { f32x4* op = (f32x4*)(out + (size_t)m * D); op[2 * lane] = h[0]; op[2 * lane + 1] = h[1]; op[128 + 2 * lane] = h[2]; op[128 + 2 * lane + 1] = h[3]; }
;             else {
;                 float s2 = 0.f;
; #pragma unroll
;                 for (int i = 0; i < 4; ++i) s2 += (h[i][0] * h[i][0] + h[i][1] * h[i][1]) + (h[i][2] * h[i][2] + h[i][3] * h[i][3]);
;                 const float rh = 1.0f / sqrtf(wave_sum(s2) * (1.0f / D) + RMS_EPS);
;                 v4u o0, o1; o0.x = pk2(h[0][0], h[0][1]); o0.y = pk2(h[0][2], h[0][3]); o0.z = pk2(h[1][0], h[1][1]); o0.w = pk2(h[1][2], h[1][3]);
;                 o1.x = pk2(h[2][0], h[2][1]); o1.y = pk2(h[2][2], h[2][3]); o1.z = pk2(h[3][0], h[3][1]); o1.w = pk2(h[3][2], h[3][3]);
;                 v4u* hp = (v4u*)(hout + (size_t)m * D); hp[lane] = o0; hp[64 + lane] = o1;
; #pragma unroll
;                 for (int i = 0; i < 4; ++i) h[i] = h[i] * rh * q4[i];
;                 o0.x = pk2(h[0][0], h[0][1]); o0.y = pk2(h[0][2], h[0][3]); o0.z = pk2(h[1][0], h[1][1]); o0.w = pk2(h[1][2], h[1][3]);
;                 o1.x = pk2(h[2][0], h[2][1]); o1.y = pk2(h[2][2], h[2][3]); o1.z = pk2(h[3][0], h[3][1]); o1.w = pk2(h[3][2], h[3][3]);
;                 v4u* up = (v4u*)(u + (size_t)m * D); up[lane] = o0; up[64 + lane] = o1;
	v_pk_mul_f32 v[52:53], v[38:39], v[38:39]
	v_pk_mul_f32 v[54:55], v[36:37], v[36:37]
	v_mul_f32_e32 v2, v44, v44
	v_pk_mov_b32 v[56:57], v[54:55], v[52:53] op_sel:[1,0]
	v_mov_b32_e32 v55, v53
	v_pk_add_f32 v[52:53], v[56:57], v[54:55]
	v_pk_mul_f32 v[54:55], v[42:43], v[42:43]
	v_pk_mul_f32 v[56:57], v[40:41], v[40:41]
	v_pk_add_f32 v[52:53], v[52:53], v[52:53] op_sel_hi:[0,1]
	v_pk_mov_b32 v[58:59], v[56:57], v[54:55] op_sel:[1,0]
	v_mov_b32_e32 v57, v55
	v_pk_add_f32 v[54:55], v[58:59], v[56:57]
	v_pk_fma_f32 v[56:57], v[44:45], v[44:45], v[2:3] op_sel_hi:[1,1,0]
	v_mul_f32_e32 v2, v46, v46
	v_pk_add_f32 v[54:55], v[54:55], v[54:55] op_sel_hi:[0,1]
	v_pk_fma_f32 v[58:59], v[46:47], v[46:47], v[2:3] op_sel_hi:[1,1,0]
	v_mul_f32_e32 v56, v48, v48
	v_mul_f32_e32 v58, v49, v49
	v_mul_f32_e32 v52, v50, v50
	v_mul_f32_e32 v54, v51, v51
	v_pk_add_f32 v[56:57], v[56:57], v[58:59]
	v_pk_add_f32 v[52:53], v[52:53], v[54:55]
	v_cvt_pk_bf16_f32 v58, v48, v49
	v_cvt_pk_bf16_f32 v59, v50, v51
	s_nop 0
	v_pk_add_f32 v[52:53], v[56:57], v[52:53]
	v_cvt_pk_bf16_f32 v57, v46, v47
	s_nop 0
	v_add_f32_e32 v2, v52, v53
	s_nop 1
	v_add_f32_dpp v2, v2, v2 quad_perm:[1,0,3,2] row_mask:0xf bank_mask:0xf bound_ctrl:1
	s_nop 1
	v_add_f32_dpp v2, v2, v2 quad_perm:[2,3,0,1] row_mask:0xf bank_mask:0xf bound_ctrl:1
	s_nop 1
	v_add_f32_dpp v2, v2, v2 row_half_mirror row_mask:0xf bank_mask:0xf bound_ctrl:1
	s_nop 1
	v_add_f32_dpp v2, v2, v2 row_mirror row_mask:0xf bank_mask:0xf bound_ctrl:1
	s_nop 0
	v_readlane_b32 s1, v2, 16
	v_readlane_b32 s4, v2, 48
	v_readlane_b32 s2, v2, 0
	v_readlane_b32 s3, v2, 32
	v_mov_b32_e32 v52, s1
	v_mov_b32_e32 v53, s4
	v_pk_add_f32 v[52:53], s[2:3], v[52:53]
	s_nop 0
	v_add_f32_e32 v2, v52, v53
	v_fmamk_f32 v2, v2, 0x3a800000, v214
	s_lshl_b64 s[2:3], s[22:23], 10
	s_lshl_b64 s[2:3], s[2:3], 1
	v_lshl_add_u64 v[60:61], v[106:107], 0, s[2:3]
	v_rsq_f32_e32 v2, v2
	s_nop 0
	v_cvt_pk_bf16_f32 v52, v36, v37
	v_cvt_pk_bf16_f32 v53, v38, v39
	v_cvt_pk_bf16_f32 v54, v40, v41
	v_cvt_pk_bf16_f32 v55, v42, v43
	v_cvt_pk_bf16_f32 v56, v44, v45
	global_store_dwordx4 v[60:61], v[52:55], off sc1 nt
	global_store_dwordx4 v[60:61], v[56:59], off offset:1024 sc1 nt
	v_pk_mul_f32 v[60:61], v[44:45], v[2:3] op_sel_hi:[1,0]
	v_pk_mul_f32 v[52:53], v[36:37], v[2:3] op_sel_hi:[1,0]
	v_pk_mul_f32 v[54:55], v[38:39], v[2:3] op_sel_hi:[1,0]
	v_pk_mul_f32 v[56:57], v[40:41], v[2:3] op_sel_hi:[1,0]
	v_pk_mul_f32 v[54:55], v[26:27], v[54:55]
	v_pk_mul_f32 v[52:53], v[24:25], v[52:53]
	v_pk_mul_f32 v[58:59], v[42:43], v[2:3] op_sel_hi:[1,0]
	v_pk_mul_f32 v[56:57], v[20:21], v[56:57]
	v_pk_mul_f32 v[60:61], v[32:33], v[60:61]
	v_pk_mul_f32 v[58:59], v[22:23], v[58:59]
	v_pk_mul_f32 v[62:63], v[46:47], v[2:3] op_sel_hi:[1,0]
	v_pk_mul_f32 v[64:65], v[48:49], v[2:3] op_sel_hi:[1,0]
	v_pk_mul_f32 v[66:67], v[50:51], v[2:3] op_sel_hi:[1,0]
	v_cvt_pk_bf16_f32 v52, v52, v53
	v_cvt_pk_bf16_f32 v53, v54, v55
	v_cvt_pk_bf16_f32 v54, v56, v57
	v_cvt_pk_bf16_f32 v55, v58, v59
	v_cvt_pk_bf16_f32 v56, v60, v61
	v_lshl_add_u64 v[60:61], v[108:109], 0, s[2:3]
	s_mov_b64 s[2:3], 0
	v_pk_mul_f32 v[62:63], v[34:35], v[62:63]
	v_pk_mul_f32 v[66:67], v[30:31], v[66:67]
	v_pk_mul_f32 v[64:65], v[28:29], v[64:65]
	v_cvt_pk_bf16_f32 v57, v62, v63
	v_cvt_pk_bf16_f32 v59, v66, v67
	s_nop 0
	v_cvt_pk_bf16_f32 v58, v64, v65
	flat_store_dwordx4 v[60:61], v[52:55] sc1
	flat_store_dwordx4 v[60:61], v[56:59] offset:1024 sc1
.LBB0_748:
	s_andn2_b64 vcc, exec, s[2:3]
	s_cbranch_vccnz .LBB0_733
	s_lshl_b64 s[2:3], s[22:23], 12
	v_lshl_add_u64 v[52:53], v[110:111], 0, s[2:3]
	global_store_dwordx4 v[52:53], v[36:39], off sc1 nt
	global_store_dwordx4 v[52:53], v[40:43], off offset:16 sc1 nt
	global_store_dwordx4 v[52:53], v[44:47], off offset:2048 sc1 nt
	global_store_dwordx4 v[52:53], v[48:51], off offset:2064 sc1 nt
	s_branch .LBB0_733

; __device__ __forceinline__ void thin_pass(const Ctx& C, const bf16* hin, bf16* hout, bf16* u, float* out, const bf16* y, const float* gpost, float cmul, const float* gpre, bool last) {
;     ...
;     for (int m0 = mstart; m0 < mend; m0 += mstep) {
;         v4u yr[RB][2], hr[RB][2];
; #pragma unroll
;         for (int b = 0; b < RB; ++b) { const v4u* yp = (const v4u*)(y + (size_t)(m0 + b) * D); const v4u* hp = (const v4u*)(hin + (size_t)(m0 + b) * D);
;             yr[b][0] = yp[lane]; yr[b][1] = yp[64 + lane]; hr[b][0] = hp[lane]; hr[b][1] = hp[64 + lane]; }
; #pragma unroll
;         for (int b = 0; b < RB; ++b) {
;             const int m = m0 + b; const v4u y0 = yr[b][0], y1 = yr[b][1], h0 = hr[b][0], h1 = hr[b][1];
;             f32x4 yv[4], h[4];
;             yv[0] = (f32x4){bf_lo(y0.x), bf_hi(y0.x), bf_lo(y0.y), bf_hi(y0.y)}; yv[1] = (f32x4){bf_lo(y0.z), bf_hi(y0.z), bf_lo(y0.w), bf_hi(y0.w)};
;             yv[2] = (f32x4){bf_lo(y1.x), bf_hi(y1.x), bf_lo(y1.y), bf_hi(y1.y)}; yv[3] = (f32x4){bf_lo(y1.z), bf_hi(y1.z), bf_lo(y1.w), bf_hi(y1.w)};
;             h[0] = (f32x4){bf_lo(h0.x), bf_hi(h0.x), bf_lo(h0.y), bf_hi(h0.y)}; h[1] = (f32x4){bf_lo(h0.z), bf_hi(h0.z), bf_lo(h0.w), bf_hi(h0.w)};
;             h[2] = (f32x4){bf_lo(h1.x), bf_hi(h1.x), bf_lo(h1.y), bf_hi(h1.y)}; h[3] = (f32x4){bf_lo(h1.z), bf_hi(h1.z), bf_lo(h1.w), bf_hi(h1.w)};
;             float ss = 0.f;
; #pragma unroll
;             for (int i = 0; i < 4; ++i) ss += (yv[i][0] * yv[i][0] + yv[i][1] * yv[i][1]) + (yv[i][2] * yv[i][2] + yv[i][3] * yv[i][3]);
;             const float ry = cmul / sqrtf(wave_sum(ss) * (1.0f / D) + RMS_EPS);
; #pragma unroll
;             for (int i = 0; i < 4; ++i) h[i] = h[i] + yv[i] * ry * g4[i];
;             if (last) { f32x4* op = (f32x4*)(out + (size_t)m * D); op[2 * lane] = h[0]; op[2 * lane + 1] = h[1]; op[128 + 2 * lane] = h[2]; op[128 + 2 * lane + 1] = h[3]; }
;             else {
;                 float s2 = 0.f;
; #pragma unroll
;                 for (int i = 0; i < 4; ++i) s2 += (h[i][0] * h[i][0] + h[i][1] * h[i][1]) + (h[i][2] * h[i][2] + h[i][3] * h[i][3]);
;                 const float rh = 1.0f / sqrtf(wave_sum(s2) * (1.0f / D) + RMS_EPS);
.LBB0_1757:
	v_lshl_add_u64 v[102:103], s[8:9], 0, v[92:93]
	v_add_co_u32_e32 v36, vcc, 0xd000000, v102
	v_lshl_add_u64 v[38:39], s[14:15], 0, v[92:93]
	s_nop 0
	v_addc_co_u32_e32 v37, vcc, 0, v103, vcc
	flat_load_dwordx4 v[84:87], v[36:37] nt
	flat_load_dwordx4 v[88:91], v[36:37] offset:1024 nt
	v_add_co_u32_e32 v40, vcc, 0x2000000, v38
	s_add_i32 s2, s6, 3
	s_nop 0
	v_addc_co_u32_e32 v41, vcc, 0, v39, vcc
	global_load_dwordx4 v[104:107], v[40:41], off nt
	global_load_dwordx4 v[108:111], v[40:41], off offset:1024 nt
	flat_load_dwordx4 v[72:75], v[36:37] offset:2048 nt
	flat_load_dwordx4 v[68:71], v[36:37] offset:3072 nt
	global_load_dwordx4 v[80:83], v[40:41], off offset:2048 nt
	global_load_dwordx4 v[76:79], v[40:41], off offset:3072 nt
	s_ashr_i32 s3, s2, 31
	v_add_co_u32_e32 v36, vcc, s91, v102
	s_lshl_b64 s[16:17], s[2:3], 11
	s_nop 0
	v_addc_co_u32_e32 v37, vcc, 0, v103, vcc
	flat_load_dwordx4 v[56:59], v[36:37] nt
	flat_load_dwordx4 v[52:55], v[36:37] offset:1024 nt
	v_add_co_u32_e32 v36, vcc, s93, v38
	v_lshl_add_u64 v[44:45], v[96:97], 0, s[16:17]
	s_nop 0
	v_addc_co_u32_e32 v37, vcc, 0, v39, vcc
	global_load_dwordx4 v[64:67], v[36:37], off nt
	global_load_dwordx4 v[60:63], v[36:37], off offset:1024 nt
	v_lshl_add_u64 v[36:37], v[94:95], 0, s[16:17]
	flat_load_dwordx4 v[40:43], v[36:37] nt
	s_nop 0
	flat_load_dwordx4 v[36:39], v[36:37] offset:1024 nt
	s_nop 0
	global_load_dwordx4 v[48:51], v[44:45], off nt
	s_nop 0
	global_load_dwordx4 v[44:47], v[44:45], off offset:1024 nt
	s_add_i32 s6, s6, s4
	s_add_u32 s8, s8, s10
	s_addc_u32 s9, s9, s11
	s_waitcnt vmcnt(0) lgkmcnt(0)
	v_lshlrev_b32_e32 v129, 16, v87
	v_lshlrev_b32_e32 v128, 16, v86
	v_lshlrev_b32_e32 v114, 16, v106
	v_and_b32_e32 v115, 0xffff0000, v106
	v_lshlrev_b32_e32 v106, 16, v84
	v_lshlrev_b32_e32 v118, 16, v107
	v_and_b32_e32 v119, 0xffff0000, v107
	v_and_b32_e32 v107, 0xffff0000, v84
	v_mul_f32_e32 v2, v106, v106
	v_lshlrev_b32_e32 v84, 16, v85
	v_lshlrev_b32_e32 v120, 16, v108
	v_and_b32_e32 v121, 0xffff0000, v108
	v_lshlrev_b32_e32 v122, 16, v109
	v_and_b32_e32 v123, 0xffff0000, v109
	v_pk_fma_f32 v[108:109], v[106:107], v[106:107], v[2:3] op_sel_hi:[1,1,0]
	v_and_b32_e32 v85, 0xffff0000, v85
	v_mul_f32_e32 v2, v84, v84
	v_and_b32_e32 v87, 0xffff0000, v87
	v_and_b32_e32 v86, 0xffff0000, v86
	v_lshlrev_b32_e32 v132, 16, v88
	v_lshlrev_b32_e32 v116, 16, v90
	v_lshlrev_b32_e32 v124, 16, v110
	v_and_b32_e32 v125, 0xffff0000, v110
	v_lshlrev_b32_e32 v126, 16, v111
	v_and_b32_e32 v127, 0xffff0000, v111
	v_pk_fma_f32 v[110:111], v[84:85], v[84:85], v[2:3] op_sel_hi:[1,1,0]
	v_pk_mul_f32 v[130:131], v[86:87], v[86:87]
	v_and_b32_e32 v133, 0xffff0000, v88
	v_mul_f32_e32 v2, v132, v132
	v_lshlrev_b32_e32 v88, 16, v89
	v_pk_fma_f32 v[130:131], v[128:129], v[128:129], v[130:131]
	v_pk_fma_f32 v[134:135], v[132:133], v[132:133], v[2:3] op_sel_hi:[1,1,0]
	v_and_b32_e32 v89, 0xffff0000, v89
	v_mul_f32_e32 v2, v88, v88
	v_mov_b32_e32 v117, v109
	v_mov_b32_e32 v138, v116
	v_mov_b32_e32 v139, v111
	v_and_b32_e32 v140, 0xffff0000, v90
	v_lshlrev_b32_e32 v90, 16, v91
	v_and_b32_e32 v91, 0xffff0000, v91
	v_pk_add_f32 v[130:131], v[130:131], v[130:131] op_sel_hi:[0,1]
	v_pk_fma_f32 v[136:137], v[88:89], v[88:89], v[2:3] op_sel_hi:[1,1,0]
	v_pk_mul_f32 v[138:139], v[116:117], v[138:139]
	v_pk_add_f32 v[108:109], v[108:109], v[110:111]
	v_mul_f32_e32 v130, v140, v140
	v_mul_f32_e32 v134, v90, v90
	v_mul_f32_e32 v136, v91, v91
	v_mov_b32_e32 v139, v109
	v_pk_add_f32 v[108:109], v[138:139], v[130:131]
	v_pk_add_f32 v[110:111], v[134:135], v[136:137]
	v_lshlrev_b32_e32 v112, 16, v104
	v_pk_add_f32 v[108:109], v[108:109], v[110:111]
	v_and_b32_e32 v113, 0xffff0000, v104
	v_add_f32_e32 v2, v108, v109
	v_lshlrev_b32_e32 v104, 16, v105
	v_and_b32_e32 v105, 0xffff0000, v105
	v_add_f32_dpp v2, v2, v2 quad_perm:[1,0,3,2] row_mask:0xf bank_mask:0xf bound_ctrl:1
	s_nop 1
	v_add_f32_dpp v2, v2, v2 quad_perm:[2,3,0,1] row_mask:0xf bank_mask:0xf bound_ctrl:1
	s_nop 1
	v_add_f32_dpp v2, v2, v2 row_half_mirror row_mask:0xf bank_mask:0xf bound_ctrl:1
	s_nop 1
	v_add_f32_dpp v2, v2, v2 row_mirror row_mask:0xf bank_mask:0xf bound_ctrl:1
	s_nop 0
	v_readlane_b32 s5, v2, 16
	v_readlane_b32 s7, v2, 48
	v_readlane_b32 s2, v2, 0
	v_readlane_b32 s3, v2, 32
	v_mov_b32_e32 v108, s5
	v_mov_b32_e32 v109, s7
	v_pk_add_f32 v[108:109], s[2:3], v[108:109]
	s_nop 0
	v_add_f32_e32 v2, v108, v109
	v_fmamk_f32 v2, v2, 0x3a800000, v214
	v_rsq_f32_e32 v2, v2
	s_nop 0
	v_pk_mul_f32 v[84:85], v[2:3], v[84:85] op_sel_hi:[0,1]
	v_pk_fma_f32 v[104:105], v[10:11], v[84:85], v[104:105]
	v_mov_b32_e32 v84, v128
	v_mov_b32_e32 v85, v86
	v_mov_b32_e32 v86, v129
	v_pk_mul_f32 v[106:107], v[2:3], v[106:107] op_sel_hi:[0,1]
	v_pk_mul_f32 v[84:85], v[2:3], v[84:85] op_sel_hi:[0,1]
	v_pk_mul_f32 v[86:87], v[2:3], v[86:87] op_sel_hi:[0,1]
	v_pk_fma_f32 v[106:107], v[8:9], v[106:107], v[112:113]
	v_pk_fma_f32 v[108:109], v[6:7], v[86:87], v[118:119]
	v_pk_fma_f32 v[112:113], v[4:5], v[84:85], v[114:115]
	v_pk_mul_f32 v[84:85], v[2:3], v[132:133] op_sel_hi:[0,1]
	v_pk_mul_f32 v[86:87], v[2:3], v[88:89] op_sel_hi:[0,1]
	v_mov_b32_e32 v117, v140
	v_pk_fma_f32 v[110:111], v[18:19], v[86:87], v[122:123]
	v_pk_fma_f32 v[114:115], v[16:17], v[84:85], v[120:121]
	v_pk_mul_f32 v[84:85], v[90:91], v[2:3] op_sel_hi:[1,0]
	v_pk_mul_f32 v[86:87], v[116:117], v[2:3] op_sel_hi:[1,0]
	v_pk_fma_f32 v[118:119], v[14:15], v[84:85], v[126:127]
	v_pk_fma_f32 v[116:117], v[12:13], v[86:87], v[124:125]
	v_pk_mul_f32 v[84:85], v[104:105], v[104:105]
	v_pk_mul_f32 v[86:87], v[106:107], v[106:107]
	v_mul_f32_e32 v2, v114, v114
	v_pk_mov_b32 v[88:89], v[86:87], v[84:85] op_sel:[1,0]
; __device__ __forceinline__ void thin_pass(const Ctx& C, const bf16* hin, bf16* hout, bf16* u, float* out, const bf16* y, const float* gpost, float cmul, const float* gpre, bool last) {
;     ...
;             const int m = m0 + b; const v4u y0 = yr[b][0], y1 = yr[b][1], h0 = hr[b][0], h1 = hr[b][1];
;             f32x4 yv[4], h[4];
;             yv[0] = (f32x4){bf_lo(y0.x), bf_hi(y0.x), bf_lo(y0.y), bf_hi(y0.y)}; yv[1] = (f32x4){bf_lo(y0.z), bf_hi(y0.z), bf_lo(y0.w), bf_hi(y0.w)};
;             yv[2] = (f32x4){bf_lo(y1.x), bf_hi(y1.x), bf_lo(y1.y), bf_hi(y1.y)}; yv[3] = (f32x4){bf_lo(y1.z), bf_hi(y1.z), bf_lo(y1.w), bf_hi(y1.w)};
;             h[0] = (f32x4){bf_lo(h0.x), bf_hi(h0.x), bf_lo(h0.y), bf_hi(h0.y)}; h[1] = (f32x4){bf_lo(h0.z), bf_hi(h0.z), bf_lo(h0.w), bf_hi(h0.w)};
;             h[2] = (f32x4){bf_lo(h1.x), bf_hi(h1.x), bf_lo(h1.y), bf_hi(h1.y)}; h[3] = (f32x4){bf_lo(h1.z), bf_hi(h1.z), bf_lo(h1.w), bf_hi(h1.w)};
;             float ss = 0.f;
; #pragma unroll
;             for (int i = 0; i < 4; ++i) ss += (yv[i][0] * yv[i][0] + yv[i][1] * yv[i][1]) + (yv[i][2] * yv[i][2] + yv[i][3] * yv[i][3]);
;             const float ry = cmul / sqrtf(wave_sum(ss) * (1.0f / D) + RMS_EPS);
;     ...
;                 float s2 = 0.f;
; #pragma unroll
;                 for (int i = 0; i < 4; ++i) s2 += (h[i][0] * h[i][0] + h[i][1] * h[i][1]) + (h[i][2] * h[i][2] + h[i][3] * h[i][3]);
;                 const float rh = 1.0f / sqrtf(wave_sum(s2) * (1.0f / D) + RMS_EPS);
;                 v4u o0, o1; o0.x = pk2(h[0][0], h[0][1]); o0.y = pk2(h[0][2], h[0][3]); o0.z = pk2(h[1][0], h[1][1]); o0.w = pk2(h[1][2], h[1][3]);
;                 o1.x = pk2(h[2][0], h[2][1]); o1.y = pk2(h[2][2], h[2][3]); o1.z = pk2(h[3][0], h[3][1]); o1.w = pk2(h[3][2], h[3][3]);
;                 v4u* hp = (v4u*)(hout + (size_t)m * D); hp[lane] = o0; hp[64 + lane] = o1;
; #pragma unroll
;                 for (int i = 0; i < 4; ++i) h[i] = h[i] * rh * q4[i];
;                 o0.x = pk2(h[0][0], h[0][1]); o0.y = pk2(h[0][2], h[0][3]); o0.z = pk2(h[1][0], h[1][1]); o0.w = pk2(h[1][2], h[1][3]);
;                 o1.x = pk2(h[2][0], h[2][1]); o1.y = pk2(h[2][2], h[2][3]); o1.z = pk2(h[3][0], h[3][1]); o1.w = pk2(h[3][2], h[3][3]);
;                 v4u* up = (v4u*)(u + (size_t)m * D); up[lane] = o0; up[64 + lane] = o1;
	v_mov_b32_e32 v87, v85
	v_pk_add_f32 v[84:85], v[88:89], v[86:87]
	v_pk_mul_f32 v[86:87], v[108:109], v[108:109]
	v_pk_mul_f32 v[88:89], v[112:113], v[112:113]
	v_pk_add_f32 v[84:85], v[84:85], v[84:85] op_sel_hi:[0,1]
	v_pk_mov_b32 v[90:91], v[88:89], v[86:87] op_sel:[1,0]
	v_mov_b32_e32 v89, v87
	v_pk_add_f32 v[86:87], v[90:91], v[88:89]
	v_pk_fma_f32 v[88:89], v[114:115], v[114:115], v[2:3] op_sel_hi:[1,1,0]
	v_mul_f32_e32 v2, v110, v110
	v_pk_add_f32 v[86:87], v[86:87], v[86:87] op_sel_hi:[0,1]
	v_pk_fma_f32 v[90:91], v[110:111], v[110:111], v[2:3] op_sel_hi:[1,1,0]
	v_mul_f32_e32 v88, v116, v116
	v_mul_f32_e32 v90, v117, v117
	v_mul_f32_e32 v84, v118, v118
	v_mul_f32_e32 v86, v119, v119
	v_pk_add_f32 v[88:89], v[88:89], v[90:91]
	v_pk_add_f32 v[84:85], v[84:85], v[86:87]
	v_cvt_pk_bf16_f32 v90, v116, v117
	v_cvt_pk_bf16_f32 v91, v118, v119
	v_lshl_add_u64 v[120:121], s[12:13], 0, v[92:93]
	v_pk_add_f32 v[84:85], v[88:89], v[84:85]
	v_cvt_pk_bf16_f32 v89, v110, v111
	v_and_b32_e32 v128, 0xffff0000, v70
	v_add_f32_e32 v2, v84, v85
	s_add_u32 s12, s12, s10
	s_addc_u32 s13, s13, s11
	v_add_f32_dpp v2, v2, v2 quad_perm:[1,0,3,2] row_mask:0xf bank_mask:0xf bound_ctrl:1
	s_add_u32 s14, s14, s10
	s_addc_u32 s15, s15, s11
	v_add_f32_dpp v2, v2, v2 quad_perm:[2,3,0,1] row_mask:0xf bank_mask:0xf bound_ctrl:1
	s_cmp_lt_i32 s6, s1
	s_nop 0
	v_add_f32_dpp v2, v2, v2 row_half_mirror row_mask:0xf bank_mask:0xf bound_ctrl:1
	s_nop 1
	v_add_f32_dpp v2, v2, v2 row_mirror row_mask:0xf bank_mask:0xf bound_ctrl:1
	s_nop 0
	v_readlane_b32 s5, v2, 16
	v_readlane_b32 s7, v2, 48
	v_readlane_b32 s2, v2, 0
	v_readlane_b32 s3, v2, 32
	v_mov_b32_e32 v84, s5
	v_mov_b32_e32 v85, s7
	v_pk_add_f32 v[84:85], s[2:3], v[84:85]
	s_nop 0
	v_add_f32_e32 v2, v84, v85
	v_fmamk_f32 v2, v2, 0x3a800000, v214
	s_mov_b32 s2, 0xb000000
	v_rsq_f32_e32 v2, v2
	s_nop 0
	v_cvt_pk_bf16_f32 v84, v106, v107
	v_cvt_pk_bf16_f32 v85, v104, v105
	v_cvt_pk_bf16_f32 v86, v112, v113
	v_cvt_pk_bf16_f32 v87, v108, v109
	v_cvt_pk_bf16_f32 v88, v114, v115
	flat_store_dwordx4 v[120:121], v[84:87] sc1 nt
	flat_store_dwordx4 v[120:121], v[88:91] offset:1024 sc1 nt
	s_nop 0
	v_pk_mul_f32 v[84:85], v[106:107], v[2:3] op_sel_hi:[1,0]
	v_pk_mul_f32 v[86:87], v[104:105], v[2:3] op_sel_hi:[1,0]
	v_pk_mul_f32 v[90:91], v[108:109], v[2:3] op_sel_hi:[1,0]
	v_pk_mul_f32 v[108:109], v[116:117], v[2:3] op_sel_hi:[1,0]
	v_pk_mul_f32 v[86:87], v[26:27], v[86:87]
	v_pk_mul_f32 v[84:85], v[24:25], v[84:85]
	v_pk_mul_f32 v[88:89], v[112:113], v[2:3] op_sel_hi:[1,0]
	v_pk_mul_f32 v[90:91], v[22:23], v[90:91]
	v_pk_mul_f32 v[104:105], v[114:115], v[2:3] op_sel_hi:[1,0]
	v_pk_mul_f32 v[108:109], v[28:29], v[108:109]
	v_pk_mul_f32 v[88:89], v[20:21], v[88:89]
	v_pk_mul_f32 v[106:107], v[110:111], v[2:3] op_sel_hi:[1,0]
	v_pk_mul_f32 v[104:105], v[32:33], v[104:105]
	v_pk_mul_f32 v[110:111], v[118:119], v[2:3] op_sel_hi:[1,0]
	v_cvt_pk_bf16_f32 v84, v84, v85
	v_cvt_pk_bf16_f32 v85, v86, v87
	v_cvt_pk_bf16_f32 v87, v90, v91
	v_cvt_pk_bf16_f32 v90, v108, v109
	v_lshlrev_b32_e32 v108, 16, v72
	v_pk_mul_f32 v[110:111], v[30:31], v[110:111]
	v_cvt_pk_bf16_f32 v86, v88, v89
	v_cvt_pk_bf16_f32 v88, v104, v105
	v_add_co_u32_e32 v104, vcc, s2, v102
	v_and_b32_e32 v109, 0xffff0000, v72
	v_mul_f32_e32 v2, v108, v108
	v_lshlrev_b32_e32 v72, 16, v73
	v_cvt_pk_bf16_f32 v91, v110, v111
	v_addc_co_u32_e32 v105, vcc, 0, v103, vcc
	v_pk_fma_f32 v[110:111], v[108:109], v[108:109], v[2:3] op_sel_hi:[1,1,0]
	v_and_b32_e32 v73, 0xffff0000, v73
	v_mul_f32_e32 v2, v72, v72
	v_lshlrev_b32_e32 v115, 16, v75
	v_lshlrev_b32_e32 v114, 16, v74
	v_and_b32_e32 v75, 0xffff0000, v75
	v_and_b32_e32 v74, 0xffff0000, v74
	v_lshlrev_b32_e32 v118, 16, v68
	v_pk_mul_f32 v[106:107], v[34:35], v[106:107]
	v_pk_fma_f32 v[112:113], v[72:73], v[72:73], v[2:3] op_sel_hi:[1,1,0]
	v_cvt_pk_bf16_f32 v89, v106, v107
	flat_store_dwordx4 v[104:105], v[84:87] sc1
	flat_store_dwordx4 v[104:105], v[88:91] offset:1024 sc1
	v_pk_mul_f32 v[116:117], v[74:75], v[74:75]
	v_lshlrev_b32_e32 v84, 16, v70
	v_and_b32_e32 v119, 0xffff0000, v68
	v_mul_f32_e32 v2, v118, v118
	v_lshlrev_b32_e32 v68, 16, v69
	v_pk_fma_f32 v[116:117], v[114:115], v[114:115], v[116:117]
	v_pk_fma_f32 v[122:123], v[118:119], v[118:119], v[2:3] op_sel_hi:[1,1,0]
	v_and_b32_e32 v69, 0xffff0000, v69
	v_mul_f32_e32 v2, v68, v68
	v_mov_b32_e32 v85, v111
	v_mov_b32_e32 v126, v84
	v_mov_b32_e32 v127, v113
	v_lshlrev_b32_e32 v70, 16, v71
	v_and_b32_e32 v71, 0xffff0000, v71
	v_pk_add_f32 v[116:117], v[116:117], v[116:117] op_sel_hi:[0,1]
	v_pk_fma_f32 v[124:125], v[68:69], v[68:69], v[2:3] op_sel_hi:[1,1,0]
	v_pk_mul_f32 v[126:127], v[84:85], v[126:127]
	v_pk_add_f32 v[110:111], v[110:111], v[112:113]
	v_mul_f32_e32 v116, v128, v128
	v_mul_f32_e32 v122, v70, v70
	v_mul_f32_e32 v124, v71, v71
	v_mov_b32_e32 v127, v111
	v_pk_add_f32 v[110:111], v[126:127], v[116:117]
	v_pk_add_f32 v[112:113], v[122:123], v[124:125]
	v_lshlrev_b32_e32 v86, 16, v80
	v_pk_add_f32 v[110:111], v[110:111], v[112:113]
	v_and_b32_e32 v87, 0xffff0000, v80
	v_add_f32_e32 v2, v110, v111
	v_lshlrev_b32_e32 v80, 16, v81
	v_and_b32_e32 v81, 0xffff0000, v81
	v_add_f32_dpp v2, v2, v2 quad_perm:[1,0,3,2] row_mask:0xf bank_mask:0xf bound_ctrl:1
	v_lshlrev_b32_e32 v90, 16, v76
	v_and_b32_e32 v91, 0xffff0000, v76
	v_add_f32_dpp v2, v2, v2 quad_perm:[2,3,0,1] row_mask:0xf bank_mask:0xf bound_ctrl:1
	v_lshlrev_b32_e32 v76, 16, v77
	v_and_b32_e32 v77, 0xffff0000, v77
	v_add_f32_dpp v2, v2, v2 row_half_mirror row_mask:0xf bank_mask:0xf bound_ctrl:1
	v_lshlrev_b32_e32 v88, 16, v82
	v_and_b32_e32 v89, 0xffff0000, v82
	v_add_f32_dpp v2, v2, v2 row_mirror row_mask:0xf bank_mask:0xf bound_ctrl:1
; __device__ __forceinline__ void thin_pass(const Ctx& C, const bf16* hin, bf16* hout, bf16* u, float* out, const bf16* y, const float* gpost, float cmul, const float* gpre, bool last) {
;     ...
;             const int m = m0 + b; const v4u y0 = yr[b][0], y1 = yr[b][1], h0 = hr[b][0], h1 = hr[b][1];
;             f32x4 yv[4], h[4];
;             yv[0] = (f32x4){bf_lo(y0.x), bf_hi(y0.x), bf_lo(y0.y), bf_hi(y0.y)}; yv[1] = (f32x4){bf_lo(y0.z), bf_hi(y0.z), bf_lo(y0.w), bf_hi(y0.w)};
;             yv[2] = (f32x4){bf_lo(y1.x), bf_hi(y1.x), bf_lo(y1.y), bf_hi(y1.y)}; yv[3] = (f32x4){bf_lo(y1.z), bf_hi(y1.z), bf_lo(y1.w), bf_hi(y1.w)};
;             h[0] = (f32x4){bf_lo(h0.x), bf_hi(h0.x), bf_lo(h0.y), bf_hi(h0.y)}; h[1] = (f32x4){bf_lo(h0.z), bf_hi(h0.z), bf_lo(h0.w), bf_hi(h0.w)};
;             h[2] = (f32x4){bf_lo(h1.x), bf_hi(h1.x), bf_lo(h1.y), bf_hi(h1.y)}; h[3] = (f32x4){bf_lo(h1.z), bf_hi(h1.z), bf_lo(h1.w), bf_hi(h1.w)};
;             float ss = 0.f;
; #pragma unroll
;             for (int i = 0; i < 4; ++i) ss += (yv[i][0] * yv[i][0] + yv[i][1] * yv[i][1]) + (yv[i][2] * yv[i][2] + yv[i][3] * yv[i][3]);
;             const float ry = cmul / sqrtf(wave_sum(ss) * (1.0f / D) + RMS_EPS);
; #pragma unroll
;             for (int i = 0; i < 4; ++i) h[i] = h[i] + yv[i] * ry * g4[i];
;             if (last) { f32x4* op = (f32x4*)(out + (size_t)m * D); op[2 * lane] = h[0]; op[2 * lane + 1] = h[1]; op[128 + 2 * lane] = h[2]; op[128 + 2 * lane + 1] = h[3]; }
;             else {
;                 float s2 = 0.f;
; #pragma unroll
;                 for (int i = 0; i < 4; ++i) s2 += (h[i][0] * h[i][0] + h[i][1] * h[i][1]) + (h[i][2] * h[i][2] + h[i][3] * h[i][3]);
;                 const float rh = 1.0f / sqrtf(wave_sum(s2) * (1.0f / D) + RMS_EPS);
;                 v4u o0, o1; o0.x = pk2(h[0][0], h[0][1]); o0.y = pk2(h[0][2], h[0][3]); o0.z = pk2(h[1][0], h[1][1]); o0.w = pk2(h[1][2], h[1][3]);
;                 o1.x = pk2(h[2][0], h[2][1]); o1.y = pk2(h[2][2], h[2][3]); o1.z = pk2(h[3][0], h[3][1]); o1.w = pk2(h[3][2], h[3][3]);
;                 v4u* hp = (v4u*)(hout + (size_t)m * D); hp[lane] = o0; hp[64 + lane] = o1;
; #pragma unroll
;                 for (int i = 0; i < 4; ++i) h[i] = h[i] * rh * q4[i];
;                 o0.x = pk2(h[0][0], h[0][1]); o0.y = pk2(h[0][2], h[0][3]); o0.z = pk2(h[1][0], h[1][1]); o0.w = pk2(h[1][2], h[1][3]);
	v_lshlrev_b32_e32 v106, 16, v78
	v_readlane_b32 s5, v2, 16
	v_readlane_b32 s7, v2, 48
	v_readlane_b32 s2, v2, 0
	v_readlane_b32 s3, v2, 32
	v_mov_b32_e32 v110, s5
	v_mov_b32_e32 v111, s7
	v_pk_add_f32 v[110:111], s[2:3], v[110:111]
	v_and_b32_e32 v107, 0xffff0000, v78
	v_add_f32_e32 v2, v110, v111
	v_fmamk_f32 v2, v2, 0x3a800000, v214
	v_lshlrev_b32_e32 v78, 16, v79
	v_and_b32_e32 v79, 0xffff0000, v79
	v_lshlrev_b32_e32 v82, 16, v83
	v_and_b32_e32 v83, 0xffff0000, v83
	v_rsq_f32_e32 v2, v2
	s_nop 0
	v_pk_mul_f32 v[72:73], v[2:3], v[72:73] op_sel_hi:[0,1]
	v_pk_mul_f32 v[108:109], v[2:3], v[108:109] op_sel_hi:[0,1]
	v_pk_fma_f32 v[80:81], v[10:11], v[72:73], v[80:81]
	v_mov_b32_e32 v72, v114
	v_mov_b32_e32 v73, v74
	v_pk_mul_f32 v[68:69], v[2:3], v[68:69] op_sel_hi:[0,1]
	v_mov_b32_e32 v85, v128
	v_pk_fma_f32 v[86:87], v[8:9], v[108:109], v[86:87]
	v_pk_mul_f32 v[72:73], v[2:3], v[72:73] op_sel_hi:[0,1]
	v_mov_b32_e32 v74, v115
	v_pk_fma_f32 v[76:77], v[18:19], v[68:69], v[76:77]
	v_pk_mul_f32 v[68:69], v[70:71], v[2:3] op_sel_hi:[1,0]
	v_pk_mul_f32 v[70:71], v[84:85], v[2:3] op_sel_hi:[1,0]
	v_pk_mul_f32 v[74:75], v[2:3], v[74:75] op_sel_hi:[0,1]
	v_pk_fma_f32 v[88:89], v[4:5], v[72:73], v[88:89]
	v_pk_mul_f32 v[72:73], v[2:3], v[118:119] op_sel_hi:[0,1]
	v_pk_fma_f32 v[84:85], v[12:13], v[70:71], v[106:107]
	v_pk_fma_f32 v[78:79], v[14:15], v[68:69], v[78:79]
	v_pk_mul_f32 v[68:69], v[80:81], v[80:81]
	v_pk_mul_f32 v[70:71], v[86:87], v[86:87]
	v_pk_fma_f32 v[82:83], v[6:7], v[74:75], v[82:83]
	v_pk_fma_f32 v[90:91], v[16:17], v[72:73], v[90:91]
	v_pk_mov_b32 v[72:73], v[70:71], v[68:69] op_sel:[1,0]
	v_mov_b32_e32 v71, v69
	v_pk_add_f32 v[68:69], v[72:73], v[70:71]
	v_pk_mul_f32 v[70:71], v[82:83], v[82:83]
	v_pk_mul_f32 v[72:73], v[88:89], v[88:89]
	v_mul_f32_e32 v2, v90, v90
	v_pk_mov_b32 v[74:75], v[72:73], v[70:71] op_sel:[1,0]
	v_mov_b32_e32 v73, v71
	v_pk_add_f32 v[70:71], v[74:75], v[72:73]
	v_pk_fma_f32 v[72:73], v[90:91], v[90:91], v[2:3] op_sel_hi:[1,1,0]
	v_mul_f32_e32 v2, v76, v76
	v_pk_add_f32 v[68:69], v[68:69], v[68:69] op_sel_hi:[0,1]
	v_pk_add_f32 v[70:71], v[70:71], v[70:71] op_sel_hi:[0,1]
	v_pk_fma_f32 v[74:75], v[76:77], v[76:77], v[2:3] op_sel_hi:[1,1,0]
	v_mul_f32_e32 v72, v84, v84
	v_mul_f32_e32 v74, v85, v85
	v_mul_f32_e32 v68, v78, v78
	v_mul_f32_e32 v70, v79, v79
	v_pk_add_f32 v[72:73], v[72:73], v[74:75]
	v_pk_add_f32 v[68:69], v[68:69], v[70:71]
	v_cvt_pk_bf16_f32 v74, v84, v85
	v_cvt_pk_bf16_f32 v75, v78, v79
	v_and_b32_e32 v108, 0xffff0000, v54
	v_pk_add_f32 v[68:69], v[72:73], v[68:69]
	v_cvt_pk_bf16_f32 v73, v76, v77
	s_nop 0
	v_add_f32_e32 v2, v68, v69
	s_nop 1
	v_add_f32_dpp v2, v2, v2 quad_perm:[1,0,3,2] row_mask:0xf bank_mask:0xf bound_ctrl:1
	s_nop 1
	v_add_f32_dpp v2, v2, v2 quad_perm:[2,3,0,1] row_mask:0xf bank_mask:0xf bound_ctrl:1
	s_nop 1
	v_add_f32_dpp v2, v2, v2 row_half_mirror row_mask:0xf bank_mask:0xf bound_ctrl:1
	s_nop 1
	v_add_f32_dpp v2, v2, v2 row_mirror row_mask:0xf bank_mask:0xf bound_ctrl:1
	s_nop 0
	v_readlane_b32 s5, v2, 16
	v_readlane_b32 s7, v2, 48
	v_readlane_b32 s2, v2, 0
	v_readlane_b32 s3, v2, 32
	v_mov_b32_e32 v68, s5
	v_mov_b32_e32 v69, s7
	v_pk_add_f32 v[68:69], s[2:3], v[68:69]
	s_nop 0
	v_add_f32_e32 v2, v68, v69
	v_fmamk_f32 v2, v2, 0x3a800000, v214
	v_rsq_f32_e32 v2, v2
	s_nop 0
	v_cvt_pk_bf16_f32 v68, v86, v87
	v_cvt_pk_bf16_f32 v69, v80, v81
	v_cvt_pk_bf16_f32 v70, v88, v89
	v_cvt_pk_bf16_f32 v71, v82, v83
	v_cvt_pk_bf16_f32 v72, v90, v91
	flat_store_dwordx4 v[120:121], v[68:71] offset:2048 sc1 nt
	flat_store_dwordx4 v[120:121], v[72:75] offset:3072 sc1 nt
	v_pk_mul_f32 v[78:79], v[78:79], v[2:3] op_sel_hi:[1,0]
	v_pk_mul_f32 v[68:69], v[86:87], v[2:3] op_sel_hi:[1,0]
	v_pk_mul_f32 v[70:71], v[80:81], v[2:3] op_sel_hi:[1,0]
	v_pk_mul_f32 v[74:75], v[82:83], v[2:3] op_sel_hi:[1,0]
	v_pk_mul_f32 v[70:71], v[26:27], v[70:71]
	v_pk_mul_f32 v[68:69], v[24:25], v[68:69]
	v_pk_mul_f32 v[74:75], v[22:23], v[74:75]
	v_pk_mul_f32 v[78:79], v[30:31], v[78:79]
	v_pk_mul_f32 v[72:73], v[88:89], v[2:3] op_sel_hi:[1,0]
	v_pk_mul_f32 v[80:81], v[90:91], v[2:3] op_sel_hi:[1,0]
	v_cvt_pk_bf16_f32 v68, v68, v69
	v_cvt_pk_bf16_f32 v69, v70, v71
	v_cvt_pk_bf16_f32 v71, v74, v75
	v_cvt_pk_bf16_f32 v75, v78, v79
	v_lshlrev_b32_e32 v78, 16, v56
	v_pk_mul_f32 v[72:73], v[20:21], v[72:73]
	v_pk_mul_f32 v[76:77], v[76:77], v[2:3] op_sel_hi:[1,0]
	v_pk_mul_f32 v[80:81], v[32:33], v[80:81]
	v_pk_mul_f32 v[82:83], v[84:85], v[2:3] op_sel_hi:[1,0]
	v_and_b32_e32 v79, 0xffff0000, v56
	v_mul_f32_e32 v2, v78, v78
	v_lshlrev_b32_e32 v56, 16, v57
	v_pk_mul_f32 v[82:83], v[28:29], v[82:83]
	v_cvt_pk_bf16_f32 v70, v72, v73
	v_cvt_pk_bf16_f32 v72, v80, v81
	v_pk_fma_f32 v[80:81], v[78:79], v[78:79], v[2:3] op_sel_hi:[1,1,0]
	v_and_b32_e32 v57, 0xffff0000, v57
	v_mul_f32_e32 v2, v56, v56
	v_lshlrev_b32_e32 v85, 16, v59
	v_lshlrev_b32_e32 v84, 16, v58
	v_and_b32_e32 v59, 0xffff0000, v59
	v_and_b32_e32 v58, 0xffff0000, v58
	v_lshlrev_b32_e32 v88, 16, v52
	v_pk_mul_f32 v[76:77], v[34:35], v[76:77]
	v_cvt_pk_bf16_f32 v74, v82, v83
	v_pk_fma_f32 v[82:83], v[56:57], v[56:57], v[2:3] op_sel_hi:[1,1,0]
	v_cvt_pk_bf16_f32 v73, v76, v77
	flat_store_dwordx4 v[104:105], v[68:71] offset:2048 sc1
	flat_store_dwordx4 v[104:105], v[72:75] offset:3072 sc1
	v_pk_mul_f32 v[86:87], v[58:59], v[58:59]
	v_lshlrev_b32_e32 v68, 16, v54
	v_and_b32_e32 v89, 0xffff0000, v52
	v_mul_f32_e32 v2, v88, v88
	v_lshlrev_b32_e32 v52, 16, v53
	v_pk_fma_f32 v[86:87], v[84:85], v[84:85], v[86:87]
	v_pk_fma_f32 v[90:91], v[88:89], v[88:89], v[2:3] op_sel_hi:[1,1,0]
	v_and_b32_e32 v53, 0xffff0000, v53
	v_mul_f32_e32 v2, v52, v52
; __device__ __forceinline__ void thin_pass(const Ctx& C, const bf16* hin, bf16* hout, bf16* u, float* out, const bf16* y, const float* gpost, float cmul, const float* gpre, bool last) {
;     ...
;             const int m = m0 + b; const v4u y0 = yr[b][0], y1 = yr[b][1], h0 = hr[b][0], h1 = hr[b][1];
;             f32x4 yv[4], h[4];
;             yv[0] = (f32x4){bf_lo(y0.x), bf_hi(y0.x), bf_lo(y0.y), bf_hi(y0.y)}; yv[1] = (f32x4){bf_lo(y0.z), bf_hi(y0.z), bf_lo(y0.w), bf_hi(y0.w)};
;             yv[2] = (f32x4){bf_lo(y1.x), bf_hi(y1.x), bf_lo(y1.y), bf_hi(y1.y)}; yv[3] = (f32x4){bf_lo(y1.z), bf_hi(y1.z), bf_lo(y1.w), bf_hi(y1.w)};
;             h[0] = (f32x4){bf_lo(h0.x), bf_hi(h0.x), bf_lo(h0.y), bf_hi(h0.y)}; h[1] = (f32x4){bf_lo(h0.z), bf_hi(h0.z), bf_lo(h0.w), bf_hi(h0.w)};
;             h[2] = (f32x4){bf_lo(h1.x), bf_hi(h1.x), bf_lo(h1.y), bf_hi(h1.y)}; h[3] = (f32x4){bf_lo(h1.z), bf_hi(h1.z), bf_lo(h1.w), bf_hi(h1.w)};
;             float ss = 0.f;
; #pragma unroll
;             for (int i = 0; i < 4; ++i) ss += (yv[i][0] * yv[i][0] + yv[i][1] * yv[i][1]) + (yv[i][2] * yv[i][2] + yv[i][3] * yv[i][3]);
;             const float ry = cmul / sqrtf(wave_sum(ss) * (1.0f / D) + RMS_EPS);
; #pragma unroll
;             for (int i = 0; i < 4; ++i) h[i] = h[i] + yv[i] * ry * g4[i];
;             if (last) { f32x4* op = (f32x4*)(out + (size_t)m * D); op[2 * lane] = h[0]; op[2 * lane + 1] = h[1]; op[128 + 2 * lane] = h[2]; op[128 + 2 * lane + 1] = h[3]; }
;             else {
;                 float s2 = 0.f;
; #pragma unroll
;                 for (int i = 0; i < 4; ++i) s2 += (h[i][0] * h[i][0] + h[i][1] * h[i][1]) + (h[i][2] * h[i][2] + h[i][3] * h[i][3]);
;                 const float rh = 1.0f / sqrtf(wave_sum(s2) * (1.0f / D) + RMS_EPS);
;                 v4u o0, o1; o0.x = pk2(h[0][0], h[0][1]); o0.y = pk2(h[0][2], h[0][3]); o0.z = pk2(h[1][0], h[1][1]); o0.w = pk2(h[1][2], h[1][3]);
;                 o1.x = pk2(h[2][0], h[2][1]); o1.y = pk2(h[2][2], h[2][3]); o1.z = pk2(h[3][0], h[3][1]); o1.w = pk2(h[3][2], h[3][3]);
;                 v4u* hp = (v4u*)(hout + (size_t)m * D); hp[lane] = o0; hp[64 + lane] = o1;
; #pragma unroll
;                 for (int i = 0; i < 4; ++i) h[i] = h[i] * rh * q4[i];
;                 o0.x = pk2(h[0][0], h[0][1]); o0.y = pk2(h[0][2], h[0][3]); o0.z = pk2(h[1][0], h[1][1]); o0.w = pk2(h[1][2], h[1][3]);
	v_mov_b32_e32 v69, v81
	v_mov_b32_e32 v106, v68
	v_mov_b32_e32 v107, v83
	v_lshlrev_b32_e32 v54, 16, v55
	v_and_b32_e32 v55, 0xffff0000, v55
	v_pk_add_f32 v[86:87], v[86:87], v[86:87] op_sel_hi:[0,1]
	v_pk_fma_f32 v[104:105], v[52:53], v[52:53], v[2:3] op_sel_hi:[1,1,0]
	v_pk_mul_f32 v[106:107], v[68:69], v[106:107]
	v_pk_add_f32 v[80:81], v[80:81], v[82:83]
	v_mul_f32_e32 v86, v108, v108
	v_mul_f32_e32 v90, v54, v54
	v_mul_f32_e32 v104, v55, v55
	v_mov_b32_e32 v107, v81
	v_pk_add_f32 v[80:81], v[106:107], v[86:87]
	v_pk_add_f32 v[82:83], v[90:91], v[104:105]
	v_lshlrev_b32_e32 v70, 16, v64
	v_pk_add_f32 v[80:81], v[80:81], v[82:83]
	v_and_b32_e32 v71, 0xffff0000, v64
	v_add_f32_e32 v2, v80, v81
	v_lshlrev_b32_e32 v64, 16, v65
	v_and_b32_e32 v65, 0xffff0000, v65
	v_add_f32_dpp v2, v2, v2 quad_perm:[1,0,3,2] row_mask:0xf bank_mask:0xf bound_ctrl:1
	v_lshlrev_b32_e32 v74, 16, v60
	v_and_b32_e32 v75, 0xffff0000, v60
	v_add_f32_dpp v2, v2, v2 quad_perm:[2,3,0,1] row_mask:0xf bank_mask:0xf bound_ctrl:1
	v_lshlrev_b32_e32 v60, 16, v61
	v_and_b32_e32 v61, 0xffff0000, v61
	v_add_f32_dpp v2, v2, v2 row_half_mirror row_mask:0xf bank_mask:0xf bound_ctrl:1
	v_lshlrev_b32_e32 v72, 16, v66
	v_and_b32_e32 v73, 0xffff0000, v66
	v_add_f32_dpp v2, v2, v2 row_mirror row_mask:0xf bank_mask:0xf bound_ctrl:1
	v_lshlrev_b32_e32 v76, 16, v62
	v_readlane_b32 s5, v2, 16
	v_readlane_b32 s7, v2, 48
	v_readlane_b32 s2, v2, 0
	v_readlane_b32 s3, v2, 32
	v_mov_b32_e32 v80, s5
	v_mov_b32_e32 v81, s7
	v_pk_add_f32 v[80:81], s[2:3], v[80:81]
	v_and_b32_e32 v77, 0xffff0000, v62
	v_add_f32_e32 v2, v80, v81
	v_fmamk_f32 v2, v2, 0x3a800000, v214
	v_lshlrev_b32_e32 v62, 16, v63
	v_and_b32_e32 v63, 0xffff0000, v63
	v_lshlrev_b32_e32 v66, 16, v67
	v_and_b32_e32 v67, 0xffff0000, v67
	v_rsq_f32_e32 v2, v2
	s_nop 0
	v_pk_mul_f32 v[56:57], v[2:3], v[56:57] op_sel_hi:[0,1]
	v_pk_mul_f32 v[78:79], v[2:3], v[78:79] op_sel_hi:[0,1]
	v_pk_fma_f32 v[64:65], v[10:11], v[56:57], v[64:65]
	v_mov_b32_e32 v56, v84
	v_mov_b32_e32 v57, v58
	v_pk_mul_f32 v[52:53], v[2:3], v[52:53] op_sel_hi:[0,1]
	v_mov_b32_e32 v69, v108
	v_pk_fma_f32 v[70:71], v[8:9], v[78:79], v[70:71]
	v_pk_mul_f32 v[56:57], v[2:3], v[56:57] op_sel_hi:[0,1]
	v_mov_b32_e32 v58, v85
	v_pk_fma_f32 v[60:61], v[18:19], v[52:53], v[60:61]
	v_pk_mul_f32 v[52:53], v[54:55], v[2:3] op_sel_hi:[1,0]
	v_pk_mul_f32 v[54:55], v[68:69], v[2:3] op_sel_hi:[1,0]
	v_pk_mul_f32 v[58:59], v[2:3], v[58:59] op_sel_hi:[0,1]
	v_pk_fma_f32 v[72:73], v[4:5], v[56:57], v[72:73]
	v_pk_mul_f32 v[56:57], v[2:3], v[88:89] op_sel_hi:[0,1]
	v_pk_fma_f32 v[68:69], v[12:13], v[54:55], v[76:77]
	v_pk_fma_f32 v[62:63], v[14:15], v[52:53], v[62:63]
	v_pk_mul_f32 v[52:53], v[64:65], v[64:65]
	v_pk_mul_f32 v[54:55], v[70:71], v[70:71]
	v_pk_fma_f32 v[66:67], v[6:7], v[58:59], v[66:67]
	v_pk_fma_f32 v[74:75], v[16:17], v[56:57], v[74:75]
	v_pk_mov_b32 v[56:57], v[54:55], v[52:53] op_sel:[1,0]
	v_mov_b32_e32 v55, v53
	v_pk_add_f32 v[52:53], v[56:57], v[54:55]
	v_pk_mul_f32 v[54:55], v[66:67], v[66:67]
	v_pk_mul_f32 v[56:57], v[72:73], v[72:73]
	v_mul_f32_e32 v2, v74, v74
	v_pk_mov_b32 v[58:59], v[56:57], v[54:55] op_sel:[1,0]
	v_mov_b32_e32 v57, v55
	v_pk_add_f32 v[54:55], v[58:59], v[56:57]
	v_pk_fma_f32 v[56:57], v[74:75], v[74:75], v[2:3] op_sel_hi:[1,1,0]
	v_mul_f32_e32 v2, v60, v60
	v_pk_add_f32 v[52:53], v[52:53], v[52:53] op_sel_hi:[0,1]
	v_pk_add_f32 v[54:55], v[54:55], v[54:55] op_sel_hi:[0,1]
	v_pk_fma_f32 v[58:59], v[60:61], v[60:61], v[2:3] op_sel_hi:[1,1,0]
	v_mul_f32_e32 v56, v68, v68
	v_mul_f32_e32 v58, v69, v69
	v_mul_f32_e32 v52, v62, v62
	v_mul_f32_e32 v54, v63, v63
	v_pk_add_f32 v[56:57], v[56:57], v[58:59]
	v_pk_add_f32 v[52:53], v[52:53], v[54:55]
	v_cvt_pk_bf16_f32 v58, v68, v69
	v_cvt_pk_bf16_f32 v59, v62, v63
	v_and_b32_e32 v80, 0xffff0000, v38
	v_pk_add_f32 v[52:53], v[56:57], v[52:53]
	v_cvt_pk_bf16_f32 v57, v60, v61
	s_nop 0
	v_add_f32_e32 v2, v52, v53
	s_nop 1
	v_add_f32_dpp v2, v2, v2 quad_perm:[1,0,3,2] row_mask:0xf bank_mask:0xf bound_ctrl:1
	s_nop 1
	v_add_f32_dpp v2, v2, v2 quad_perm:[2,3,0,1] row_mask:0xf bank_mask:0xf bound_ctrl:1
	s_nop 1
	v_add_f32_dpp v2, v2, v2 row_half_mirror row_mask:0xf bank_mask:0xf bound_ctrl:1
	s_nop 1
	v_add_f32_dpp v2, v2, v2 row_mirror row_mask:0xf bank_mask:0xf bound_ctrl:1
	s_nop 0
	v_readlane_b32 s5, v2, 16
	v_readlane_b32 s7, v2, 48
	v_readlane_b32 s2, v2, 0
	v_readlane_b32 s3, v2, 32
	v_mov_b32_e32 v52, s5
	v_mov_b32_e32 v53, s7
	v_pk_add_f32 v[52:53], s[2:3], v[52:53]
	s_nop 0
	v_add_f32_e32 v2, v52, v53
	v_fmamk_f32 v2, v2, 0x3a800000, v214
	s_mov_b32 s2, 0xb001000
	v_add_co_u32_e32 v76, vcc, s84, v120
	v_rsq_f32_e32 v2, v2
	s_nop 0
	v_cvt_pk_bf16_f32 v52, v70, v71
	v_cvt_pk_bf16_f32 v53, v64, v65
	v_cvt_pk_bf16_f32 v54, v72, v73
	v_cvt_pk_bf16_f32 v55, v66, v67
	s_nop 0
	v_addc_co_u32_e32 v77, vcc, 0, v121, vcc
	v_cvt_pk_bf16_f32 v56, v74, v75
	flat_store_dwordx4 v[76:77], v[52:55] sc1 nt
	flat_store_dwordx4 v[76:77], v[56:59] offset:1024 sc1 nt
	v_pk_mul_f32 v[62:63], v[62:63], v[2:3] op_sel_hi:[1,0]
	v_pk_mul_f32 v[52:53], v[70:71], v[2:3] op_sel_hi:[1,0]
	v_pk_mul_f32 v[54:55], v[64:65], v[2:3] op_sel_hi:[1,0]
	v_pk_mul_f32 v[58:59], v[66:67], v[2:3] op_sel_hi:[1,0]
	v_pk_mul_f32 v[54:55], v[26:27], v[54:55]
	v_pk_mul_f32 v[52:53], v[24:25], v[52:53]
	v_pk_mul_f32 v[56:57], v[72:73], v[2:3] op_sel_hi:[1,0]
	v_pk_mul_f32 v[58:59], v[22:23], v[58:59]
	v_pk_mul_f32 v[60:61], v[60:61], v[2:3] op_sel_hi:[1,0]
	v_pk_mul_f32 v[62:63], v[30:31], v[62:63]
	v_pk_mul_f32 v[56:57], v[20:21], v[56:57]
	v_pk_mul_f32 v[64:65], v[74:75], v[2:3] op_sel_hi:[1,0]
	v_pk_mul_f32 v[60:61], v[34:35], v[60:61]
; __device__ __forceinline__ unsigned pk2(float lo, float hi) { unsigned r; asm("v_cvt_pk_bf16_f32 %0, %1, %2" : "=v"(r) : "v"(lo), "v"(hi)); return r; }
; __device__ __forceinline__ void thin_pass(const Ctx& C, const bf16* hin, bf16* hout, bf16* u, float* out, const bf16* y, const float* gpost, float cmul, const float* gpre, bool last) {
;     ...
;             const int m = m0 + b; const v4u y0 = yr[b][0], y1 = yr[b][1], h0 = hr[b][0], h1 = hr[b][1];
;             f32x4 yv[4], h[4];
;             yv[0] = (f32x4){bf_lo(y0.x), bf_hi(y0.x), bf_lo(y0.y), bf_hi(y0.y)}; yv[1] = (f32x4){bf_lo(y0.z), bf_hi(y0.z), bf_lo(y0.w), bf_hi(y0.w)};
;             yv[2] = (f32x4){bf_lo(y1.x), bf_hi(y1.x), bf_lo(y1.y), bf_hi(y1.y)}; yv[3] = (f32x4){bf_lo(y1.z), bf_hi(y1.z), bf_lo(y1.w), bf_hi(y1.w)};
;             h[0] = (f32x4){bf_lo(h0.x), bf_hi(h0.x), bf_lo(h0.y), bf_hi(h0.y)}; h[1] = (f32x4){bf_lo(h0.z), bf_hi(h0.z), bf_lo(h0.w), bf_hi(h0.w)};
;             h[2] = (f32x4){bf_lo(h1.x), bf_hi(h1.x), bf_lo(h1.y), bf_hi(h1.y)}; h[3] = (f32x4){bf_lo(h1.z), bf_hi(h1.z), bf_lo(h1.w), bf_hi(h1.w)};
;             float ss = 0.f;
; #pragma unroll
;             for (int i = 0; i < 4; ++i) ss += (yv[i][0] * yv[i][0] + yv[i][1] * yv[i][1]) + (yv[i][2] * yv[i][2] + yv[i][3] * yv[i][3]);
;             const float ry = cmul / sqrtf(wave_sum(ss) * (1.0f / D) + RMS_EPS);
;     ...
;                 for (int i = 0; i < 4; ++i) h[i] = h[i] * rh * q4[i];
;                 o0.x = pk2(h[0][0], h[0][1]); o0.y = pk2(h[0][2], h[0][3]); o0.z = pk2(h[1][0], h[1][1]); o0.w = pk2(h[1][2], h[1][3]);
;                 o1.x = pk2(h[2][0], h[2][1]); o1.y = pk2(h[2][2], h[2][3]); o1.z = pk2(h[3][0], h[3][1]); o1.w = pk2(h[3][2], h[3][3]);
;                 v4u* up = (v4u*)(u + (size_t)m * D); up[lane] = o0; up[64 + lane] = o1;
	v_cvt_pk_bf16_f32 v52, v52, v53
	v_cvt_pk_bf16_f32 v53, v54, v55
	v_cvt_pk_bf16_f32 v55, v58, v59
	v_cvt_pk_bf16_f32 v59, v62, v63
	v_lshlrev_b32_e32 v62, 16, v40
	v_pk_mul_f32 v[64:65], v[32:33], v[64:65]
	v_pk_mul_f32 v[66:67], v[68:69], v[2:3] op_sel_hi:[1,0]
	v_cvt_pk_bf16_f32 v54, v56, v57
	v_cvt_pk_bf16_f32 v57, v60, v61
	v_add_co_u32_e32 v60, vcc, s2, v102
	v_and_b32_e32 v63, 0xffff0000, v40
	v_mul_f32_e32 v2, v62, v62
	v_lshlrev_b32_e32 v40, 16, v41
	v_pk_mul_f32 v[66:67], v[28:29], v[66:67]
	v_cvt_pk_bf16_f32 v56, v64, v65
	v_addc_co_u32_e32 v61, vcc, 0, v103, vcc
	v_pk_fma_f32 v[64:65], v[62:63], v[62:63], v[2:3] op_sel_hi:[1,1,0]
	v_and_b32_e32 v41, 0xffff0000, v41
	v_mul_f32_e32 v2, v40, v40
	v_lshlrev_b32_e32 v69, 16, v43
	v_lshlrev_b32_e32 v68, 16, v42
	v_and_b32_e32 v43, 0xffff0000, v43
	v_and_b32_e32 v42, 0xffff0000, v42
	v_lshlrev_b32_e32 v72, 16, v36
	v_cvt_pk_bf16_f32 v58, v66, v67
	flat_store_dwordx4 v[60:61], v[52:55] sc1
	flat_store_dwordx4 v[60:61], v[56:59] offset:1024 sc1
	v_pk_fma_f32 v[66:67], v[40:41], v[40:41], v[2:3] op_sel_hi:[1,1,0]
	v_lshlrev_b32_e32 v52, 16, v38
	v_pk_mul_f32 v[70:71], v[42:43], v[42:43]
	v_and_b32_e32 v73, 0xffff0000, v36
	v_mul_f32_e32 v2, v72, v72
	v_lshlrev_b32_e32 v36, 16, v37
	v_pk_fma_f32 v[70:71], v[68:69], v[68:69], v[70:71]
	v_pk_fma_f32 v[74:75], v[72:73], v[72:73], v[2:3] op_sel_hi:[1,1,0]
	v_and_b32_e32 v37, 0xffff0000, v37
	v_mul_f32_e32 v2, v36, v36
	v_mov_b32_e32 v53, v65
	v_mov_b32_e32 v78, v52
	v_mov_b32_e32 v79, v67
	v_lshlrev_b32_e32 v38, 16, v39
	v_and_b32_e32 v39, 0xffff0000, v39
	v_pk_add_f32 v[70:71], v[70:71], v[70:71] op_sel_hi:[0,1]
	v_pk_fma_f32 v[76:77], v[36:37], v[36:37], v[2:3] op_sel_hi:[1,1,0]
	v_pk_mul_f32 v[78:79], v[52:53], v[78:79]
	v_pk_add_f32 v[64:65], v[64:65], v[66:67]
	v_mul_f32_e32 v70, v80, v80
	v_mul_f32_e32 v74, v38, v38
	v_mul_f32_e32 v76, v39, v39
	v_mov_b32_e32 v79, v65
	v_pk_add_f32 v[64:65], v[78:79], v[70:71]
	v_pk_add_f32 v[66:67], v[74:75], v[76:77]
	v_lshlrev_b32_e32 v54, 16, v48
	v_pk_add_f32 v[64:65], v[64:65], v[66:67]
	v_and_b32_e32 v55, 0xffff0000, v48
	v_add_f32_e32 v2, v64, v65
	v_lshlrev_b32_e32 v48, 16, v49
	v_and_b32_e32 v49, 0xffff0000, v49
	v_add_f32_dpp v2, v2, v2 quad_perm:[1,0,3,2] row_mask:0xf bank_mask:0xf bound_ctrl:1
	v_lshlrev_b32_e32 v58, 16, v44
	v_and_b32_e32 v59, 0xffff0000, v44
	v_add_f32_dpp v2, v2, v2 quad_perm:[2,3,0,1] row_mask:0xf bank_mask:0xf bound_ctrl:1
	v_lshlrev_b32_e32 v44, 16, v45
	v_and_b32_e32 v45, 0xffff0000, v45
	v_add_f32_dpp v2, v2, v2 row_half_mirror row_mask:0xf bank_mask:0xf bound_ctrl:1
	v_lshlrev_b32_e32 v56, 16, v50
	v_and_b32_e32 v57, 0xffff0000, v50
	v_add_f32_dpp v2, v2, v2 row_mirror row_mask:0xf bank_mask:0xf bound_ctrl:1
	v_lshlrev_b32_e32 v50, 16, v51
	v_readlane_b32 s5, v2, 16
	v_readlane_b32 s7, v2, 48
	v_readlane_b32 s2, v2, 0
	v_readlane_b32 s3, v2, 32
	v_mov_b32_e32 v64, s5
	v_mov_b32_e32 v65, s7
	v_pk_add_f32 v[64:65], s[2:3], v[64:65]
	v_and_b32_e32 v51, 0xffff0000, v51
	v_add_f32_e32 v2, v64, v65
	v_fmamk_f32 v2, v2, 0x3a800000, v214
	v_lshlrev_b32_e32 v60, 16, v46
	v_and_b32_e32 v61, 0xffff0000, v46
	v_lshlrev_b32_e32 v46, 16, v47
	v_and_b32_e32 v47, 0xffff0000, v47
	v_rsq_f32_e32 v2, v2
	s_nop 0
	v_pk_mul_f32 v[40:41], v[2:3], v[40:41] op_sel_hi:[0,1]
	v_pk_mul_f32 v[62:63], v[2:3], v[62:63] op_sel_hi:[0,1]
	v_pk_fma_f32 v[48:49], v[10:11], v[40:41], v[48:49]
	v_mov_b32_e32 v40, v69
	v_mov_b32_e32 v41, v43
	v_pk_mul_f32 v[36:37], v[2:3], v[36:37] op_sel_hi:[0,1]
	v_mov_b32_e32 v53, v80
	v_pk_fma_f32 v[54:55], v[8:9], v[62:63], v[54:55]
	v_pk_mul_f32 v[40:41], v[2:3], v[40:41] op_sel_hi:[0,1]
	v_mov_b32_e32 v69, v42
	v_pk_fma_f32 v[44:45], v[18:19], v[36:37], v[44:45]
	v_pk_mul_f32 v[36:37], v[38:39], v[2:3] op_sel_hi:[1,0]
; __device__ __forceinline__ unsigned pk2(float lo, float hi) { unsigned r; asm("v_cvt_pk_bf16_f32 %0, %1, %2" : "=v"(r) : "v"(lo), "v"(hi)); return r; }
; __device__ __forceinline__ void thin_pass(const Ctx& C, const bf16* hin, bf16* hout, bf16* u, float* out, const bf16* y, const float* gpost, float cmul, const float* gpre, bool last) {
;     ...
;                 float s2 = 0.f;
; #pragma unroll
;                 for (int i = 0; i < 4; ++i) s2 += (h[i][0] * h[i][0] + h[i][1] * h[i][1]) + (h[i][2] * h[i][2] + h[i][3] * h[i][3]);
;                 const float rh = 1.0f / sqrtf(wave_sum(s2) * (1.0f / D) + RMS_EPS);
;                 v4u o0, o1; o0.x = pk2(h[0][0], h[0][1]); o0.y = pk2(h[0][2], h[0][3]); o0.z = pk2(h[1][0], h[1][1]); o0.w = pk2(h[1][2], h[1][3]);
;                 o1.x = pk2(h[2][0], h[2][1]); o1.y = pk2(h[2][2], h[2][3]); o1.z = pk2(h[3][0], h[3][1]); o1.w = pk2(h[3][2], h[3][3]);
;                 v4u* hp = (v4u*)(hout + (size_t)m * D); hp[lane] = o0; hp[64 + lane] = o1;
; #pragma unroll
;                 for (int i = 0; i < 4; ++i) h[i] = h[i] * rh * q4[i];
;                 o0.x = pk2(h[0][0], h[0][1]); o0.y = pk2(h[0][2], h[0][3]); o0.z = pk2(h[1][0], h[1][1]); o0.w = pk2(h[1][2], h[1][3]);
;                 o1.x = pk2(h[2][0], h[2][1]); o1.y = pk2(h[2][2], h[2][3]); o1.z = pk2(h[3][0], h[3][1]); o1.w = pk2(h[3][2], h[3][3]);
;                 v4u* up = (v4u*)(u + (size_t)m * D); up[lane] = o0; up[64 + lane] = o1;
	v_pk_mul_f32 v[38:39], v[52:53], v[2:3] op_sel_hi:[1,0]
	v_pk_mul_f32 v[42:43], v[2:3], v[68:69] op_sel_hi:[0,1]
	v_pk_fma_f32 v[50:51], v[6:7], v[40:41], v[50:51]
	v_pk_mul_f32 v[40:41], v[2:3], v[72:73] op_sel_hi:[0,1]
	v_pk_fma_f32 v[52:53], v[12:13], v[38:39], v[60:61]
	v_pk_fma_f32 v[46:47], v[14:15], v[36:37], v[46:47]
	v_pk_mul_f32 v[36:37], v[48:49], v[48:49]
	v_pk_mul_f32 v[38:39], v[54:55], v[54:55]
	v_pk_fma_f32 v[56:57], v[4:5], v[42:43], v[56:57]
	v_pk_fma_f32 v[58:59], v[16:17], v[40:41], v[58:59]
	v_pk_mov_b32 v[40:41], v[38:39], v[36:37] op_sel:[1,0]
	v_mov_b32_e32 v39, v37
	v_pk_add_f32 v[36:37], v[40:41], v[38:39]
	v_pk_mul_f32 v[38:39], v[50:51], v[50:51]
	v_pk_mul_f32 v[40:41], v[56:57], v[56:57]
	v_mul_f32_e32 v2, v58, v58
	v_pk_mov_b32 v[42:43], v[40:41], v[38:39] op_sel:[1,0]
	v_mov_b32_e32 v41, v39
	v_pk_add_f32 v[38:39], v[42:43], v[40:41]
	v_pk_fma_f32 v[40:41], v[58:59], v[58:59], v[2:3] op_sel_hi:[1,1,0]
	v_mul_f32_e32 v2, v44, v44
	v_pk_add_f32 v[36:37], v[36:37], v[36:37] op_sel_hi:[0,1]
	v_pk_add_f32 v[38:39], v[38:39], v[38:39] op_sel_hi:[0,1]
	v_pk_fma_f32 v[42:43], v[44:45], v[44:45], v[2:3] op_sel_hi:[1,1,0]
	v_mul_f32_e32 v40, v52, v52
	v_mul_f32_e32 v42, v53, v53
	v_mul_f32_e32 v36, v46, v46
	v_mul_f32_e32 v38, v47, v47
	v_pk_add_f32 v[40:41], v[40:41], v[42:43]
	v_pk_add_f32 v[36:37], v[36:37], v[38:39]
	v_lshl_add_u64 v[60:61], v[98:99], 0, s[16:17]
	v_pk_add_f32 v[36:37], v[40:41], v[36:37]
	v_cvt_pk_bf16_f32 v41, v44, v45
	v_cvt_pk_bf16_f32 v42, v52, v53
	v_cvt_pk_bf16_f32 v43, v46, v47
	s_nop 0
	v_add_f32_e32 v2, v36, v37
	s_nop 1
	v_add_f32_dpp v2, v2, v2 quad_perm:[1,0,3,2] row_mask:0xf bank_mask:0xf bound_ctrl:1
	s_nop 1
	v_add_f32_dpp v2, v2, v2 quad_perm:[2,3,0,1] row_mask:0xf bank_mask:0xf bound_ctrl:1
	s_nop 1
	v_add_f32_dpp v2, v2, v2 row_half_mirror row_mask:0xf bank_mask:0xf bound_ctrl:1
	s_nop 1
	v_add_f32_dpp v2, v2, v2 row_mirror row_mask:0xf bank_mask:0xf bound_ctrl:1
	s_nop 0
	v_readlane_b32 s5, v2, 16
	v_readlane_b32 s7, v2, 48
	v_readlane_b32 s2, v2, 0
	v_readlane_b32 s3, v2, 32
	v_mov_b32_e32 v36, s5
	v_mov_b32_e32 v37, s7
	v_pk_add_f32 v[36:37], s[2:3], v[36:37]
	s_nop 0
	v_add_f32_e32 v2, v36, v37
	v_fmamk_f32 v2, v2, 0x3a800000, v214
	v_rsq_f32_e32 v2, v2
	s_nop 0
	v_cvt_pk_bf16_f32 v36, v54, v55
	v_cvt_pk_bf16_f32 v37, v48, v49
	v_cvt_pk_bf16_f32 v38, v56, v57
	v_cvt_pk_bf16_f32 v39, v50, v51
	v_cvt_pk_bf16_f32 v40, v58, v59
	flat_store_dwordx4 v[60:61], v[36:39] sc1 nt
	flat_store_dwordx4 v[60:61], v[40:43] offset:1024 sc1 nt
	v_pk_mul_f32 v[44:45], v[44:45], v[2:3] op_sel_hi:[1,0]
	v_pk_mul_f32 v[36:37], v[54:55], v[2:3] op_sel_hi:[1,0]
	v_pk_mul_f32 v[38:39], v[48:49], v[2:3] op_sel_hi:[1,0]
	v_pk_mul_f32 v[40:41], v[56:57], v[2:3] op_sel_hi:[1,0]
	v_pk_mul_f32 v[38:39], v[26:27], v[38:39]
	v_pk_mul_f32 v[36:37], v[24:25], v[36:37]
	v_pk_mul_f32 v[42:43], v[50:51], v[2:3] op_sel_hi:[1,0]
	v_pk_mul_f32 v[40:41], v[20:21], v[40:41]
	v_pk_mul_f32 v[44:45], v[34:35], v[44:45]
	v_pk_mul_f32 v[42:43], v[22:23], v[42:43]
	v_pk_mul_f32 v[48:49], v[58:59], v[2:3] op_sel_hi:[1,0]
	v_pk_mul_f32 v[50:51], v[52:53], v[2:3] op_sel_hi:[1,0]
	v_pk_mul_f32 v[46:47], v[46:47], v[2:3] op_sel_hi:[1,0]
	v_cvt_pk_bf16_f32 v36, v36, v37
	v_cvt_pk_bf16_f32 v37, v38, v39
	v_cvt_pk_bf16_f32 v38, v40, v41
	v_cvt_pk_bf16_f32 v39, v42, v43
	v_cvt_pk_bf16_f32 v41, v44, v45
	v_lshl_add_u64 v[44:45], v[100:101], 0, s[16:17]
	v_pk_mul_f32 v[48:49], v[32:33], v[48:49]
	v_pk_mul_f32 v[46:47], v[30:31], v[46:47]
	v_pk_mul_f32 v[50:51], v[28:29], v[50:51]
	v_cvt_pk_bf16_f32 v40, v48, v49
	v_cvt_pk_bf16_f32 v43, v46, v47
	s_nop 0
	v_cvt_pk_bf16_f32 v42, v50, v51
	flat_store_dwordx4 v[44:45], v[36:39] sc1
	flat_store_dwordx4 v[44:45], v[40:43] offset:1024 sc1
	s_cbranch_scc1 .LBB0_1757
